# attention PV segments: each transition lgkmcnt(0) swapped with the following MFMA whose operands the previous wait already covered (36 sites, pure reorder)
# speedup vs baseline: 1.0344x; 1.0011x over previous
.LBB0_1141:
	ds_read_b128 v[66:69], v205 offset:49152
	ds_read_b128 v[70:73], v205 offset:57344
	ds_read_b128 v[222:225], v206 offset:49152
	ds_read_b128 v[226:229], v206 offset:57344
	v_exp_f32_e32 v1, v156
	v_exp_f32_e32 v156, v157
	s_waitcnt lgkmcnt(3)
	v_mfma_f32_32x32x16_bf16 v[82:97], v[66:69], v[126:129], 0
	v_exp_f32_e32 v157, v160
	v_exp_f32_e32 v160, v161
	v_add_f32_e32 v161, 0, v177
	v_add_f32_e32 v161, v220, v161
	v_add_f32_e32 v161, v163, v161
	v_add_f32_e32 v161, v217, v161
	v_add_f32_e32 v161, v164, v161
	s_waitcnt lgkmcnt(2)
	v_mfma_f32_32x32x16_bf16 v[66:81], v[70:73], v[126:129], 0
	v_add_f32_e32 v161, v176, v161
	v_add_f32_e32 v161, v165, v161
	v_add_f32_e32 v161, v175, v161
	v_add_f32_e32 v161, v172, v161
	v_add_f32_e32 v161, v174, v161
	v_add_f32_e32 v161, v171, v161
	v_add_f32_e32 v161, v173, v161
	s_waitcnt lgkmcnt(1)
	v_mfma_f32_32x32x16_bf16 v[82:97], v[222:225], v[114:117], v[82:97]
	v_add_f32_e32 v161, v168, v161
	v_add_f32_e32 v161, v170, v161
	v_exp_f32_e32 v154, v154
	v_add_f32_e32 v161, v167, v161
	v_exp_f32_e32 v155, v155
	v_add_f32_e32 v161, v169, v161
	v_exp_f32_e32 v150, v150
	s_waitcnt lgkmcnt(0)
	v_mfma_f32_32x32x16_bf16 v[66:81], v[226:229], v[114:117], v[66:81]
	ds_read_b128 v[222:225], v207 offset:49152
	ds_read_b128 v[226:229], v207 offset:57344
	v_add_f32_e32 v161, v1, v161
	v_exp_f32_e32 v151, v151
	v_add_f32_e32 v161, v156, v161
	v_exp_f32_e32 v148, v148
	v_add_f32_e32 v161, v154, v161
	v_exp_f32_e32 v149, v149
	s_waitcnt lgkmcnt(1)
	v_mfma_f32_32x32x16_bf16 v[82:97], v[222:225], v[118:121], v[82:97]
	v_add_f32_e32 v161, v155, v161
	v_exp_f32_e32 v146, v146
	v_add_f32_e32 v161, v150, v161
	v_exp_f32_e32 v147, v147
	v_add_f32_e32 v161, v151, v161
	v_add_f32_e32 v161, v148, v161
	v_add_f32_e32 v161, v149, v161
	s_waitcnt lgkmcnt(0)
	v_mfma_f32_32x32x16_bf16 v[66:81], v[226:229], v[118:121], v[66:81]
	ds_read_b128 v[222:225], v208 offset:49152
	ds_read_b128 v[226:229], v208 offset:57344
	v_exp_f32_e32 v158, v158
	v_add_f32_e32 v161, v146, v161
	v_exp_f32_e32 v159, v159
	v_add_f32_e32 v161, v147, v161
	v_exp_f32_e32 v152, v152
	v_add_f32_e32 v161, v157, v161
	s_waitcnt lgkmcnt(1)
	v_mfma_f32_32x32x16_bf16 v[82:97], v[222:225], v[122:125], v[82:97]
	v_exp_f32_e32 v153, v153
	v_add_f32_e32 v161, v160, v161
	v_add_f32_e32 v161, v158, v161
	v_add_f32_e32 v161, v159, v161
	v_add_f32_e32 v161, v152, v161
	v_add_f32_e32 v214, v153, v161
	v_mov_b32_e32 v215, v214
	s_waitcnt lgkmcnt(0)
	v_mfma_f32_32x32x16_bf16 v[66:81], v[226:229], v[122:125], v[66:81]
	ds_read_b128 v[222:225], v209 offset:49152
	ds_read_b128 v[226:229], v209 offset:57344
	v_permlane32_swap_b32_e32 v214, v215
	s_waitcnt lgkmcnt(1)
	v_mfma_f32_32x32x16_bf16 v[82:97], v[222:225], v[110:113], v[82:97]
	s_waitcnt lgkmcnt(0)
	v_mfma_f32_32x32x16_bf16 v[66:81], v[226:229], v[110:113], v[66:81]
	ds_read_b128 v[222:225], v210 offset:49152
	ds_read_b128 v[226:229], v210 offset:57344
	s_waitcnt lgkmcnt(1)
	v_mfma_f32_32x32x16_bf16 v[82:97], v[222:225], v[106:109], v[82:97]
	s_waitcnt lgkmcnt(0)
	v_mfma_f32_32x32x16_bf16 v[66:81], v[226:229], v[106:109], v[66:81]
	ds_read_b128 v[222:225], v211 offset:49152
	ds_read_b128 v[226:229], v211 offset:57344
	s_waitcnt lgkmcnt(1)
	v_mfma_f32_32x32x16_bf16 v[82:97], v[222:225], v[102:105], v[82:97]
	s_waitcnt lgkmcnt(0)
	v_mfma_f32_32x32x16_bf16 v[66:81], v[226:229], v[102:105], v[66:81]
	ds_read_b128 v[222:225], v212 offset:49152
	ds_read_b128 v[226:229], v212 offset:57344
	v_cvt_pk_bf16_f32 v162, v177, v220
	v_cvt_pk_bf16_f32 v163, v163, v217
	v_cvt_pk_bf16_f32 v164, v164, v176
	v_cvt_pk_bf16_f32 v165, v165, v175
	v_cvt_pk_bf16_f32 v172, v172, v174
	v_cvt_pk_bf16_f32 v173, v171, v173
	s_waitcnt lgkmcnt(1)
	v_mfma_f32_32x32x16_bf16 v[82:97], v[222:225], v[98:101], v[82:97]
	v_cvt_pk_bf16_f32 v174, v168, v170
	v_cvt_pk_bf16_f32 v175, v167, v169
	v_cvt_pk_bf16_f32 v168, v1, v156
	v_cvt_pk_bf16_f32 v169, v154, v155
	v_cvt_pk_bf16_f32 v170, v150, v151
	v_cvt_pk_bf16_f32 v171, v148, v149
	v_cvt_pk_bf16_f32 v216, v146, v147
	s_waitcnt lgkmcnt(0)
	v_mfma_f32_32x32x16_bf16 v[66:81], v[226:229], v[98:101], v[66:81]
	v_cvt_pk_bf16_f32 v217, v157, v160
	v_cvt_pk_bf16_f32 v218, v158, v159
	v_permlane32_swap_b32_e32 v162, v164
	v_cvt_pk_bf16_f32 v219, v152, v153
	v_permlane32_swap_b32_e32 v216, v218
	v_permlane32_swap_b32_e32 v163, v165
	v_permlane32_swap_b32_e32 v172, v174
	v_permlane32_swap_b32_e32 v173, v175
	v_permlane32_swap_b32_e32 v168, v170
	v_permlane32_swap_b32_e32 v169, v171
	v_permlane32_swap_b32_e32 v217, v219
	v_lshl_add_u64 v[154:155], s[16:17], 0, v[188:189]
	v_add_co_u32_e32 v146, vcc, s23, v154
	v_lshl_add_u64 v[156:157], s[16:17], 0, v[190:191]
	s_nop 0
	v_addc_co_u32_e32 v147, vcc, 0, v155, vcc
	v_add_co_u32_e32 v150, vcc, s23, v156
	s_nop 1
	v_addc_co_u32_e32 v151, vcc, 0, v157, vcc
	v_add_co_u32_e32 v154, vcc, s24, v154
	global_load_dwordx4 v[146:149], v[146:147], off
	s_nop 0
	global_load_dwordx4 v[150:153], v[150:151], off
	v_addc_co_u32_e32 v155, vcc, 0, v155, vcc
	v_add_co_u32_e32 v158, vcc, s24, v156
	s_nop 1
	v_addc_co_u32_e32 v159, vcc, 0, v157, vcc
	global_load_dwordx4 v[154:157], v[154:155], off
	s_nop 0
	global_load_dwordx4 v[158:161], v[158:159], off
	ds_read_b64_tr_b16 v[220:221], v199 offset:0
	ds_read_b64_tr_b16 v[222:223], v199 offset:0x800
	ds_read_b64_tr_b16 v[224:225], v199 offset:0x1000
	ds_read_b64_tr_b16 v[226:227], v199 offset:0x1800
	ds_read_b64_tr_b16 v[228:229], v199 offset:0x2000
	ds_read_b64_tr_b16 v[230:231], v199 offset:0x2800
	ds_read_b64_tr_b16 v[232:233], v199 offset:0x3000
	ds_read_b64_tr_b16 v[234:235], v199 offset:0x3800
	s_waitcnt lgkmcnt(0)
	s_nop 0
	v_mfma_f32_32x32x16_bf16 v[18:33], v[162:165], v[220:223], v[18:33]
	ds_read_b64_tr_b16 v[220:221], v199 offset:0x200
	ds_read_b64_tr_b16 v[222:223], v199 offset:0xa00
	v_mfma_f32_32x32x16_bf16 v[18:33], v[172:175], v[224:227], v[18:33]
	ds_read_b64_tr_b16 v[224:225], v199 offset:0x1200
	ds_read_b64_tr_b16 v[226:227], v199 offset:0x1a00
	v_mfma_f32_32x32x16_bf16 v[18:33], v[168:171], v[228:231], v[18:33]
	ds_read_b64_tr_b16 v[228:229], v199 offset:0x2200
	ds_read_b64_tr_b16 v[230:231], v199 offset:0x2a00
	ds_read_b64_tr_b16 v[236:237], v199 offset:0x3200
	ds_read_b64_tr_b16 v[238:239], v199 offset:0x3a00
	v_mfma_f32_32x32x16_bf16 v[18:33], v[216:219], v[232:235], v[18:33]
	s_waitcnt lgkmcnt(0)
	v_mfma_f32_32x32x16_bf16 v[50:65], v[162:165], v[220:223], v[50:65]
	ds_read_b64_tr_b16 v[220:221], v199 offset:0x400
	ds_read_b64_tr_b16 v[222:223], v199 offset:0xc00
	v_mfma_f32_32x32x16_bf16 v[50:65], v[172:175], v[224:227], v[50:65]
	ds_read_b64_tr_b16 v[224:225], v199 offset:0x1400
	ds_read_b64_tr_b16 v[226:227], v199 offset:0x1c00
	v_mfma_f32_32x32x16_bf16 v[50:65], v[168:171], v[228:231], v[50:65]
	ds_read_b64_tr_b16 v[228:229], v199 offset:0x2400
	ds_read_b64_tr_b16 v[230:231], v199 offset:0x2c00
	ds_read_b64_tr_b16 v[232:233], v199 offset:0x3400
	ds_read_b64_tr_b16 v[234:235], v199 offset:0x3c00
	v_mfma_f32_32x32x16_bf16 v[50:65], v[216:219], v[236:239], v[50:65]
	s_waitcnt lgkmcnt(0)
	v_mfma_f32_32x32x16_bf16 v[34:49], v[162:165], v[220:223], v[34:49]
	ds_read_b64_tr_b16 v[220:221], v199 offset:0x600
	ds_read_b64_tr_b16 v[222:223], v199 offset:0xe00
	v_mfma_f32_32x32x16_bf16 v[34:49], v[172:175], v[224:227], v[34:49]
	ds_read_b64_tr_b16 v[224:225], v199 offset:0x1600
	ds_read_b64_tr_b16 v[226:227], v199 offset:0x1e00
	v_mfma_f32_32x32x16_bf16 v[34:49], v[168:171], v[228:231], v[34:49]
	ds_read_b64_tr_b16 v[228:229], v199 offset:0x2600
	ds_read_b64_tr_b16 v[230:231], v199 offset:0x2e00
	ds_read_b64_tr_b16 v[236:237], v199 offset:0x3600
	ds_read_b64_tr_b16 v[238:239], v199 offset:0x3e00
	v_mfma_f32_32x32x16_bf16 v[34:49], v[216:219], v[232:235], v[34:49]
	s_waitcnt lgkmcnt(0)
	v_mfma_f32_32x32x16_bf16 v[2:17], v[162:165], v[220:223], v[2:17]
	v_max_f32_e32 v1, v83, v83
	v_max_f32_e32 v167, v82, v82
	v_max_f32_e32 v1, v167, v1
	v_max3_f32 v1, v1, v84, v85
	v_max3_f32 v1, v1, v86, v87
	v_max3_f32 v1, v1, v88, v89
	v_max3_f32 v1, v1, v90, v91
	v_max3_f32 v1, v1, v92, v93
	v_mfma_f32_32x32x16_bf16 v[2:17], v[172:175], v[224:227], v[2:17]
	v_max3_f32 v1, v1, v94, v95
	v_max3_f32 v1, v1, v96, v97
	v_max3_f32 v1, v1, v66, v67
	v_max3_f32 v1, v1, v68, v69
	v_max3_f32 v1, v1, v70, v71
	v_max3_f32 v1, v1, v72, v73
	v_max3_f32 v1, v1, v74, v75
	v_max3_f32 v1, v1, v76, v77
	v_mfma_f32_32x32x16_bf16 v[2:17], v[168:171], v[228:231], v[2:17]
	v_max3_f32 v1, v1, v78, v79
	v_max3_f32 v1, v1, v80, v81
	v_mov_b32_e32 v162, v1
	s_nop 1
	v_permlane32_swap_b32_e32 v1, v162
	v_max_f32_e32 v162, v162, v162
	v_max_f32_e32 v1, v1, v1
	v_max_f32_e32 v1, v1, v162
	v_max_f32_e32 v162, v166, v166
	v_max_f32_e32 v162, v162, v1
	v_sub_f32_e32 v163, v1, v166
	v_mfma_f32_32x32x16_bf16 v[2:17], v[216:219], v[236:239], v[2:17]
	v_sub_f32_e32 v1, v166, v162
	v_mul_f32_e32 v1, 0x3e0293ee, v1
	v_exp_f32_e32 v1, v1
	v_cmp_ge_f32_e32 vcc, s22, v163
	s_cmp_eq_u64 vcc, exec
	s_cselect_b64 s[2:3], -1, 0
	s_barrier
	s_waitcnt vmcnt(4)
	v_cndmask_b32_e64 v216, v1, 1.0, s[2:3]
	v_cmp_gt_f32_e32 vcc, 1.0, v216
	s_waitcnt vmcnt(4)
	ds_write_b128 v203, v[130:133]
	ds_write_b128 v204, v[134:137]
	ds_write_b128 v201, v[138:141] offset:32768
	ds_write_b128 v202, v[142:145] offset:32768
	s_cmp_lt_u32 s79, 33
	s_cbranch_scc0 .Lil_end
	s_cmp_eq_u32 s89, 0
	s_cbranch_scc1 .Lil_issue
	v_lshlrev_b32_e32 v242, 4, v254
	v_add_u32_e32 v242, s87, v242
	v_lshlrev_b32_e32 v243, 3, v254
	v_add_u32_e32 v243, s88, v243
	s_bitcmp1_b32 s79, 0
	s_cbranch_scc0 .Lil_c1
	ds_read_b64 v[244:245], v242 offset:0
	ds_read_b64 v[246:247], v242 offset:1024
	ds_read_b64 v[248:249], v242 offset:2048
	ds_read_b64 v[250:251], v242 offset:3072
	s_waitcnt lgkmcnt(3)
	v_mul_f32_e32 v244, 0x41800000, v244
	v_mul_f32_e32 v245, 0x41800000, v245
	v_max_f32_e32 v244, 0xc3e00000, v244
	v_max_f32_e32 v245, 0xc3e00000, v245
	v_min_f32_e32 v244, 0x43e00000, v244
	v_min_f32_e32 v245, 0x43e00000, v245
	s_waitcnt lgkmcnt(2)
	v_mul_f32_e32 v246, 0x41800000, v246
	v_mul_f32_e32 v247, 0x41800000, v247
	v_max_f32_e32 v246, 0xc3e00000, v246
	v_max_f32_e32 v247, 0xc3e00000, v247
	v_min_f32_e32 v246, 0x43e00000, v246
	v_min_f32_e32 v247, 0x43e00000, v247
	s_waitcnt lgkmcnt(1)
	v_mul_f32_e32 v248, 0x41800000, v248
	v_mul_f32_e32 v249, 0x41800000, v249
	v_max_f32_e32 v248, 0xc3e00000, v248
	v_max_f32_e32 v249, 0xc3e00000, v249
	v_min_f32_e32 v248, 0x43e00000, v248
	v_min_f32_e32 v249, 0x43e00000, v249
	s_waitcnt lgkmcnt(0)
	v_mul_f32_e32 v250, 0x41800000, v250
	v_mul_f32_e32 v251, 0x41800000, v251
	v_max_f32_e32 v250, 0xc3e00000, v250
	v_max_f32_e32 v251, 0xc3e00000, v251
	v_min_f32_e32 v250, 0x43e00000, v250
	v_min_f32_e32 v251, 0x43e00000, v251
	v_cvt_pk_fp8_f32 v252, v244, v246
	v_cvt_pk_fp8_f32 v253, v245, v247
	v_cvt_pk_fp8_f32 v252, v248, v250 op_sel:[0,0,1]
	v_cvt_pk_fp8_f32 v253, v249, v251 op_sel:[0,0,1]
	s_nop 0
	ds_write_b32 v243, v252 offset:0
	ds_write_b32 v243, v253 offset:512
	ds_read_b64 v[244:245], v242 offset:4096
	ds_read_b64 v[246:247], v242 offset:5120
	ds_read_b64 v[248:249], v242 offset:6144
	ds_read_b64 v[250:251], v242 offset:7168
	s_waitcnt lgkmcnt(3)
	v_mul_f32_e32 v244, 0x41800000, v244
	v_mul_f32_e32 v245, 0x41800000, v245
	v_max_f32_e32 v244, 0xc3e00000, v244
	v_max_f32_e32 v245, 0xc3e00000, v245
	v_min_f32_e32 v244, 0x43e00000, v244
	v_min_f32_e32 v245, 0x43e00000, v245
	s_waitcnt lgkmcnt(2)
	v_mul_f32_e32 v246, 0x41800000, v246
	v_mul_f32_e32 v247, 0x41800000, v247
	v_max_f32_e32 v246, 0xc3e00000, v246
	v_max_f32_e32 v247, 0xc3e00000, v247
	v_min_f32_e32 v246, 0x43e00000, v246
	v_min_f32_e32 v247, 0x43e00000, v247
	s_waitcnt lgkmcnt(1)
	v_mul_f32_e32 v248, 0x41800000, v248
	v_mul_f32_e32 v249, 0x41800000, v249
	v_max_f32_e32 v248, 0xc3e00000, v248
	v_max_f32_e32 v249, 0xc3e00000, v249
	v_min_f32_e32 v248, 0x43e00000, v248
	v_min_f32_e32 v249, 0x43e00000, v249
	s_waitcnt lgkmcnt(0)
	v_mul_f32_e32 v250, 0x41800000, v250
	v_mul_f32_e32 v251, 0x41800000, v251
	v_max_f32_e32 v250, 0xc3e00000, v250
	v_max_f32_e32 v251, 0xc3e00000, v251
	v_min_f32_e32 v250, 0x43e00000, v250
	v_min_f32_e32 v251, 0x43e00000, v251
	v_cvt_pk_fp8_f32 v252, v244, v246
	v_cvt_pk_fp8_f32 v253, v245, v247
	v_cvt_pk_fp8_f32 v252, v248, v250 op_sel:[0,0,1]
	v_cvt_pk_fp8_f32 v253, v249, v251 op_sel:[0,0,1]
	s_nop 0
	ds_write_b32 v243, v252 offset:4
	ds_write_b32 v243, v253 offset:516
	ds_read_b64 v[244:245], v242 offset:8
	ds_read_b64 v[246:247], v242 offset:1032
	ds_read_b64 v[248:249], v242 offset:2056
	ds_read_b64 v[250:251], v242 offset:3080
	s_waitcnt lgkmcnt(3)
	v_mul_f32_e32 v244, 0x41800000, v244
	v_mul_f32_e32 v245, 0x41800000, v245
	v_max_f32_e32 v244, 0xc3e00000, v244
	v_max_f32_e32 v245, 0xc3e00000, v245
	v_min_f32_e32 v244, 0x43e00000, v244
	v_min_f32_e32 v245, 0x43e00000, v245
	s_waitcnt lgkmcnt(2)
	v_mul_f32_e32 v246, 0x41800000, v246
	v_mul_f32_e32 v247, 0x41800000, v247
	v_max_f32_e32 v246, 0xc3e00000, v246
	v_max_f32_e32 v247, 0xc3e00000, v247
	v_min_f32_e32 v246, 0x43e00000, v246
	v_min_f32_e32 v247, 0x43e00000, v247
	s_waitcnt lgkmcnt(1)
	v_mul_f32_e32 v248, 0x41800000, v248
	v_mul_f32_e32 v249, 0x41800000, v249
	v_max_f32_e32 v248, 0xc3e00000, v248
	v_max_f32_e32 v249, 0xc3e00000, v249
	v_min_f32_e32 v248, 0x43e00000, v248
	v_min_f32_e32 v249, 0x43e00000, v249
	s_waitcnt lgkmcnt(0)
	v_mul_f32_e32 v250, 0x41800000, v250
	v_mul_f32_e32 v251, 0x41800000, v251
	v_max_f32_e32 v250, 0xc3e00000, v250
	v_max_f32_e32 v251, 0xc3e00000, v251
	v_min_f32_e32 v250, 0x43e00000, v250
	v_min_f32_e32 v251, 0x43e00000, v251
	v_cvt_pk_fp8_f32 v252, v244, v246
	v_cvt_pk_fp8_f32 v253, v245, v247
	v_cvt_pk_fp8_f32 v252, v248, v250 op_sel:[0,0,1]
	v_cvt_pk_fp8_f32 v253, v249, v251 op_sel:[0,0,1]
	s_nop 0
	ds_write_b32 v243, v252 offset:1024
	ds_write_b32 v243, v253 offset:1536
	ds_read_b64 v[244:245], v242 offset:4104
	ds_read_b64 v[246:247], v242 offset:5128
	ds_read_b64 v[248:249], v242 offset:6152
	ds_read_b64 v[250:251], v242 offset:7176
	s_waitcnt lgkmcnt(3)
	v_mul_f32_e32 v244, 0x41800000, v244
	v_mul_f32_e32 v245, 0x41800000, v245
	v_max_f32_e32 v244, 0xc3e00000, v244
	v_max_f32_e32 v245, 0xc3e00000, v245
	v_min_f32_e32 v244, 0x43e00000, v244
	v_min_f32_e32 v245, 0x43e00000, v245
	s_waitcnt lgkmcnt(2)
	v_mul_f32_e32 v246, 0x41800000, v246
	v_mul_f32_e32 v247, 0x41800000, v247
	v_max_f32_e32 v246, 0xc3e00000, v246
	v_max_f32_e32 v247, 0xc3e00000, v247
	v_min_f32_e32 v246, 0x43e00000, v246
	v_min_f32_e32 v247, 0x43e00000, v247
	s_waitcnt lgkmcnt(1)
	v_mul_f32_e32 v248, 0x41800000, v248
	v_mul_f32_e32 v249, 0x41800000, v249
	v_max_f32_e32 v248, 0xc3e00000, v248
	v_max_f32_e32 v249, 0xc3e00000, v249
	v_min_f32_e32 v248, 0x43e00000, v248
	v_min_f32_e32 v249, 0x43e00000, v249
	s_waitcnt lgkmcnt(0)
	v_mul_f32_e32 v250, 0x41800000, v250
	v_mul_f32_e32 v251, 0x41800000, v251
	v_max_f32_e32 v250, 0xc3e00000, v250
	v_max_f32_e32 v251, 0xc3e00000, v251
	v_min_f32_e32 v250, 0x43e00000, v250
	v_min_f32_e32 v251, 0x43e00000, v251
	v_cvt_pk_fp8_f32 v252, v244, v246
	v_cvt_pk_fp8_f32 v253, v245, v247
	v_cvt_pk_fp8_f32 v252, v248, v250 op_sel:[0,0,1]
	v_cvt_pk_fp8_f32 v253, v249, v251 op_sel:[0,0,1]
	s_nop 0
	ds_write_b32 v243, v252 offset:1028
	ds_write_b32 v243, v253 offset:1540
	s_branch .Lil_issue

.LBB0_1147:
	ds_read_b64_tr_b16 v[220:221], v198 offset:0
	ds_read_b64_tr_b16 v[222:223], v198 offset:0x800
	ds_read_b64_tr_b16 v[224:225], v198 offset:0x1000
	ds_read_b64_tr_b16 v[226:227], v198 offset:0x1800
	ds_read_b64_tr_b16 v[228:229], v198 offset:0x2000
	ds_read_b64_tr_b16 v[230:231], v198 offset:0x2800
	ds_read_b64_tr_b16 v[232:233], v198 offset:0x3000
	ds_read_b64_tr_b16 v[234:235], v198 offset:0x3800
	s_waitcnt lgkmcnt(0)
	s_nop 0
	v_mfma_f32_32x32x16_bf16 v[18:33], v[162:165], v[220:223], v[18:33]
	ds_read_b64_tr_b16 v[220:221], v198 offset:0x200
	ds_read_b64_tr_b16 v[222:223], v198 offset:0xa00
	v_mfma_f32_32x32x16_bf16 v[18:33], v[166:169], v[224:227], v[18:33]
	ds_read_b64_tr_b16 v[224:225], v198 offset:0x1200
	ds_read_b64_tr_b16 v[226:227], v198 offset:0x1a00
	v_mfma_f32_32x32x16_bf16 v[18:33], v[170:173], v[228:231], v[18:33]
	ds_read_b64_tr_b16 v[228:229], v198 offset:0x2200
	ds_read_b64_tr_b16 v[230:231], v198 offset:0x2a00
	ds_read_b64_tr_b16 v[236:237], v198 offset:0x3200
	ds_read_b64_tr_b16 v[238:239], v198 offset:0x3a00
	v_mfma_f32_32x32x16_bf16 v[18:33], v[174:177], v[232:235], v[18:33]
	s_waitcnt lgkmcnt(0)
	v_mfma_f32_32x32x16_bf16 v[50:65], v[162:165], v[220:223], v[50:65]
	ds_read_b64_tr_b16 v[220:221], v198 offset:0x400
	ds_read_b64_tr_b16 v[222:223], v198 offset:0xc00
	v_mfma_f32_32x32x16_bf16 v[50:65], v[166:169], v[224:227], v[50:65]
	ds_read_b64_tr_b16 v[224:225], v198 offset:0x1400
	ds_read_b64_tr_b16 v[226:227], v198 offset:0x1c00
	v_mfma_f32_32x32x16_bf16 v[50:65], v[170:173], v[228:231], v[50:65]
	ds_read_b64_tr_b16 v[228:229], v198 offset:0x2400
	ds_read_b64_tr_b16 v[230:231], v198 offset:0x2c00
	ds_read_b64_tr_b16 v[232:233], v198 offset:0x3400
	ds_read_b64_tr_b16 v[234:235], v198 offset:0x3c00
	v_mfma_f32_32x32x16_bf16 v[50:65], v[174:177], v[236:239], v[50:65]
	s_waitcnt lgkmcnt(0)
	v_mfma_f32_32x32x16_bf16 v[34:49], v[162:165], v[220:223], v[34:49]
	ds_read_b64_tr_b16 v[220:221], v198 offset:0x600
	ds_read_b64_tr_b16 v[222:223], v198 offset:0xe00
	v_mfma_f32_32x32x16_bf16 v[34:49], v[166:169], v[224:227], v[34:49]
	ds_read_b64_tr_b16 v[224:225], v198 offset:0x1600
	ds_read_b64_tr_b16 v[226:227], v198 offset:0x1e00
	v_mfma_f32_32x32x16_bf16 v[34:49], v[170:173], v[228:231], v[34:49]
	ds_read_b64_tr_b16 v[228:229], v198 offset:0x2600
	ds_read_b64_tr_b16 v[230:231], v198 offset:0x2e00
	ds_read_b64_tr_b16 v[236:237], v198 offset:0x3600
	ds_read_b64_tr_b16 v[238:239], v198 offset:0x3e00
	v_mfma_f32_32x32x16_bf16 v[34:49], v[174:177], v[232:235], v[34:49]
	s_waitcnt lgkmcnt(0)
	v_mfma_f32_32x32x16_bf16 v[2:17], v[162:165], v[220:223], v[2:17]
	v_max_f32_e32 v1, v83, v83
	v_max_f32_e32 v200, v82, v82
	v_max_f32_e32 v1, v200, v1
	v_max3_f32 v1, v1, v84, v85
	v_max3_f32 v1, v1, v86, v87
	v_max3_f32 v1, v1, v88, v89
	v_max3_f32 v1, v1, v90, v91
	v_max3_f32 v1, v1, v92, v93
	v_mfma_f32_32x32x16_bf16 v[2:17], v[166:169], v[224:227], v[2:17]
	v_max3_f32 v1, v1, v94, v95
	v_max3_f32 v1, v1, v96, v97
	v_max3_f32 v1, v1, v66, v67
	v_max3_f32 v1, v1, v68, v69
	v_max3_f32 v1, v1, v70, v71
	v_max3_f32 v1, v1, v72, v73
	v_max3_f32 v1, v1, v74, v75
	v_max3_f32 v1, v1, v76, v77
	v_mfma_f32_32x32x16_bf16 v[2:17], v[170:173], v[228:231], v[2:17]
	v_max3_f32 v1, v1, v78, v79
	v_max3_f32 v1, v1, v80, v81
	v_mov_b32_e32 v162, v1
	s_nop 1
	v_permlane32_swap_b32_e32 v1, v162
	v_max_f32_e32 v162, v162, v162
	v_max_f32_e32 v1, v1, v1
	v_max_f32_e32 v1, v1, v162
	v_max_f32_e32 v163, v217, v217
	v_max_f32_e32 v163, v163, v1
	v_sub_f32_e32 v162, v1, v217
	v_mfma_f32_32x32x16_bf16 v[2:17], v[174:177], v[236:239], v[2:17]
	v_sub_f32_e32 v1, v217, v163
	v_mul_f32_e32 v1, 0x3e0293ee, v1
	v_exp_f32_e32 v1, v1
	v_cmp_ge_f32_e32 vcc, s22, v162
	s_cmp_eq_u64 vcc, exec
	s_cselect_b64 s[2:3], -1, 0
	s_barrier
	s_cmp_eq_u32 s89, 0
	s_cbranch_scc1 .Lil_w2a
	s_waitcnt vmcnt(12)
	s_branch .Lil_w2b

.LBB0_1153:
	ds_read_b128 v[66:69], v205 offset:49152
	ds_read_b128 v[70:73], v205 offset:57344
	v_exp_f32_e32 v1, v156
	v_exp_f32_e32 v156, v157
	v_exp_f32_e32 v154, v154
	s_waitcnt lgkmcnt(1)
	v_mfma_f32_32x32x16_bf16 v[82:97], v[66:69], v[126:129], 0
	v_exp_f32_e32 v155, v155
	v_exp_f32_e32 v150, v150
	s_waitcnt lgkmcnt(0)
	v_mfma_f32_32x32x16_bf16 v[66:81], v[70:73], v[126:129], 0
	ds_read_b128 v[126:129], v206 offset:49152
	ds_read_b128 v[130:133], v206 offset:57344
	ds_read_b128 v[134:137], v207 offset:49152
	ds_read_b128 v[138:141], v207 offset:57344
	s_waitcnt lgkmcnt(3)
	v_mfma_f32_32x32x16_bf16 v[82:97], v[126:129], v[114:117], v[82:97]
	ds_read_b128 v[126:129], v208 offset:49152
	ds_read_b128 v[142:145], v208 offset:57344
	ds_read_b128 v[184:187], v209 offset:49152
	ds_read_b128 v[188:191], v209 offset:57344
	ds_read_b128 v[200:203], v210 offset:49152
	ds_read_b128 v[204:207], v210 offset:57344
	ds_read_b128 v[222:225], v211 offset:49152
	ds_read_b128 v[208:211], v211 offset:57344
	s_waitcnt lgkmcnt(10)
	v_mfma_f32_32x32x16_bf16 v[66:81], v[130:133], v[114:117], v[66:81]
	ds_read_b128 v[114:117], v212 offset:49152
	ds_read_b128 v[130:133], v212 offset:57344
	s_waitcnt lgkmcnt(11)
	v_mfma_f32_32x32x16_bf16 v[82:97], v[134:137], v[118:121], v[82:97]
	v_exp_f32_e32 v134, v151
	v_exp_f32_e32 v135, v148
	v_exp_f32_e32 v136, v149
	v_exp_f32_e32 v137, v146
	v_exp_f32_e32 v146, v147
	v_exp_f32_e32 v147, v160
	v_exp_f32_e32 v148, v161
	s_waitcnt lgkmcnt(10)
	v_mfma_f32_32x32x16_bf16 v[66:81], v[138:141], v[118:121], v[66:81]
	v_add_f32_e32 v118, 0, v177
	v_add_f32_e32 v118, v220, v118
	v_add_f32_e32 v118, v163, v118
	v_add_f32_e32 v118, v217, v118
	v_add_f32_e32 v118, v164, v118
	v_add_f32_e32 v118, v176, v118
	v_add_f32_e32 v118, v165, v118
	s_waitcnt lgkmcnt(9)
	v_mfma_f32_32x32x16_bf16 v[82:97], v[126:129], v[122:125], v[82:97]
	v_add_f32_e32 v118, v175, v118
	v_add_f32_e32 v118, v172, v118
	v_add_f32_e32 v118, v174, v118
	v_add_f32_e32 v118, v171, v118
	v_add_f32_e32 v118, v173, v118
	v_add_f32_e32 v118, v168, v118
	v_add_f32_e32 v118, v170, v118
	s_waitcnt lgkmcnt(8)
	v_mfma_f32_32x32x16_bf16 v[66:81], v[142:145], v[122:125], v[66:81]
	v_add_f32_e32 v118, v167, v118
	v_add_f32_e32 v118, v169, v118
	v_add_f32_e32 v118, v1, v118
	v_add_f32_e32 v118, v156, v118
	v_add_f32_e32 v118, v154, v118
	v_add_f32_e32 v118, v155, v118
	v_add_f32_e32 v118, v150, v118
	s_waitcnt lgkmcnt(7)
	v_mfma_f32_32x32x16_bf16 v[82:97], v[184:187], v[110:113], v[82:97]
	v_add_f32_e32 v118, v134, v118
	v_add_f32_e32 v118, v135, v118
	v_add_f32_e32 v118, v136, v118
	v_exp_f32_e32 v138, v158
	v_exp_f32_e32 v139, v159
	v_exp_f32_e32 v140, v152
	v_exp_f32_e32 v141, v153
	s_waitcnt lgkmcnt(6)
	v_mfma_f32_32x32x16_bf16 v[66:81], v[188:191], v[110:113], v[66:81]
	v_add_f32_e32 v110, v137, v118
	v_add_f32_e32 v110, v146, v110
	v_add_f32_e32 v110, v147, v110
	v_add_f32_e32 v110, v148, v110
	v_add_f32_e32 v110, v138, v110
	v_add_f32_e32 v110, v139, v110
	v_add_f32_e32 v110, v140, v110
	s_waitcnt lgkmcnt(5)
	v_mfma_f32_32x32x16_bf16 v[82:97], v[200:203], v[106:109], v[82:97]
	v_add_f32_e32 v110, v141, v110
	v_mov_b32_e32 v111, v110
	s_nop 1
	v_permlane32_swap_b32_e32 v110, v111
	v_cvt_pk_bf16_f32 v118, v177, v220
	v_cvt_pk_bf16_f32 v119, v163, v217
	v_cvt_pk_bf16_f32 v120, v164, v176
	s_waitcnt lgkmcnt(4)
	v_mfma_f32_32x32x16_bf16 v[66:81], v[204:207], v[106:109], v[66:81]
	v_cvt_pk_bf16_f32 v121, v165, v175
	v_cvt_pk_bf16_f32 v106, v172, v174
	v_cvt_pk_bf16_f32 v107, v171, v173
	v_cvt_pk_bf16_f32 v108, v168, v170
	v_cvt_pk_bf16_f32 v109, v167, v169
	v_cvt_pk_bf16_f32 v122, v1, v156
	v_cvt_pk_bf16_f32 v123, v154, v155
	s_waitcnt lgkmcnt(3)
	v_mfma_f32_32x32x16_bf16 v[82:97], v[222:225], v[102:105], v[82:97]
	v_cvt_pk_bf16_f32 v124, v150, v134
	v_cvt_pk_bf16_f32 v125, v135, v136
	v_permlane32_swap_b32_e32 v118, v120
	v_permlane32_swap_b32_e32 v119, v121
	v_permlane32_swap_b32_e32 v106, v108
	s_waitcnt lgkmcnt(2)
	v_mfma_f32_32x32x16_bf16 v[66:81], v[208:211], v[102:105], v[66:81]
	v_cvt_pk_bf16_f32 v102, v137, v146
	v_cvt_pk_bf16_f32 v103, v147, v148
	v_cvt_pk_bf16_f32 v104, v138, v139
	v_cvt_pk_bf16_f32 v105, v140, v141
	v_permlane32_swap_b32_e32 v107, v109
	v_permlane32_swap_b32_e32 v122, v124
	s_waitcnt lgkmcnt(1)
	v_mfma_f32_32x32x16_bf16 v[82:97], v[114:117], v[98:101], v[82:97]
	v_permlane32_swap_b32_e32 v123, v125
	v_permlane32_swap_b32_e32 v102, v104
	v_permlane32_swap_b32_e32 v103, v105
	s_waitcnt lgkmcnt(0)
	v_mfma_f32_32x32x16_bf16 v[66:81], v[130:133], v[98:101], v[66:81]
	ds_read_b64_tr_b16 v[98:99], v199 offset:0
	ds_read_b64_tr_b16 v[100:101], v199 offset:0x800
	ds_read_b64_tr_b16 v[112:113], v199 offset:0x1000
	ds_read_b64_tr_b16 v[114:115], v199 offset:0x1800
	ds_read_b64_tr_b16 v[126:127], v199 offset:0x2000
	ds_read_b64_tr_b16 v[128:129], v199 offset:0x2800
	ds_read_b64_tr_b16 v[130:131], v199 offset:0x3000
	ds_read_b64_tr_b16 v[132:133], v199 offset:0x3800
	s_waitcnt lgkmcnt(0)
	s_nop 0
	v_mfma_f32_32x32x16_bf16 v[18:33], v[118:121], v[98:101], v[18:33]
	ds_read_b64_tr_b16 v[98:99], v199 offset:0x200
	ds_read_b64_tr_b16 v[100:101], v199 offset:0xa00
	v_mfma_f32_32x32x16_bf16 v[18:33], v[106:109], v[112:115], v[18:33]
	ds_read_b64_tr_b16 v[112:113], v199 offset:0x1200
	ds_read_b64_tr_b16 v[114:115], v199 offset:0x1a00
	v_mfma_f32_32x32x16_bf16 v[18:33], v[122:125], v[126:129], v[18:33]
	ds_read_b64_tr_b16 v[126:127], v199 offset:0x2200
	ds_read_b64_tr_b16 v[128:129], v199 offset:0x2a00
	ds_read_b64_tr_b16 v[134:135], v199 offset:0x3200
	ds_read_b64_tr_b16 v[136:137], v199 offset:0x3a00
	v_mfma_f32_32x32x16_bf16 v[18:33], v[102:105], v[130:133], v[18:33]
	s_waitcnt lgkmcnt(0)
	v_mfma_f32_32x32x16_bf16 v[50:65], v[118:121], v[98:101], v[50:65]
	ds_read_b64_tr_b16 v[98:99], v199 offset:0x400
	ds_read_b64_tr_b16 v[100:101], v199 offset:0xc00
	v_mfma_f32_32x32x16_bf16 v[50:65], v[106:109], v[112:115], v[50:65]
	ds_read_b64_tr_b16 v[112:113], v199 offset:0x1400
	ds_read_b64_tr_b16 v[114:115], v199 offset:0x1c00
	v_mfma_f32_32x32x16_bf16 v[50:65], v[122:125], v[126:129], v[50:65]
	ds_read_b64_tr_b16 v[126:127], v199 offset:0x2400
	ds_read_b64_tr_b16 v[128:129], v199 offset:0x2c00
	ds_read_b64_tr_b16 v[130:131], v199 offset:0x3400
	ds_read_b64_tr_b16 v[132:133], v199 offset:0x3c00
	v_mfma_f32_32x32x16_bf16 v[50:65], v[102:105], v[134:137], v[50:65]
	s_waitcnt lgkmcnt(0)
	v_mfma_f32_32x32x16_bf16 v[34:49], v[118:121], v[98:101], v[34:49]
	ds_read_b64_tr_b16 v[98:99], v199 offset:0x600
	ds_read_b64_tr_b16 v[100:101], v199 offset:0xe00
	v_mfma_f32_32x32x16_bf16 v[34:49], v[106:109], v[112:115], v[34:49]
	ds_read_b64_tr_b16 v[112:113], v199 offset:0x1600
	ds_read_b64_tr_b16 v[114:115], v199 offset:0x1e00
	v_mfma_f32_32x32x16_bf16 v[34:49], v[122:125], v[126:129], v[34:49]
	ds_read_b64_tr_b16 v[126:127], v199 offset:0x2600
	ds_read_b64_tr_b16 v[128:129], v199 offset:0x2e00
	ds_read_b64_tr_b16 v[134:135], v199 offset:0x3600
	ds_read_b64_tr_b16 v[136:137], v199 offset:0x3e00
	v_mfma_f32_32x32x16_bf16 v[34:49], v[102:105], v[130:133], v[34:49]
	s_waitcnt lgkmcnt(0)
	v_mfma_f32_32x32x16_bf16 v[2:17], v[118:121], v[98:101], v[2:17]
	v_max_f32_e32 v1, v83, v83
	v_max_f32_e32 v116, v82, v82
	v_max_f32_e32 v1, v116, v1
	v_max3_f32 v1, v1, v84, v85
	v_max3_f32 v1, v1, v86, v87
	v_max3_f32 v1, v1, v88, v89
	v_max3_f32 v1, v1, v90, v91
	v_max3_f32 v1, v1, v92, v93
	v_mfma_f32_32x32x16_bf16 v[2:17], v[106:109], v[112:115], v[2:17]
	v_max3_f32 v1, v1, v94, v95
	v_max3_f32 v1, v1, v96, v97
	v_max3_f32 v1, v1, v66, v67
	v_max3_f32 v1, v1, v68, v69
	v_max3_f32 v1, v1, v70, v71
	v_max3_f32 v1, v1, v72, v73
	v_max3_f32 v1, v1, v74, v75
	v_max3_f32 v1, v1, v76, v77
	v_mfma_f32_32x32x16_bf16 v[2:17], v[122:125], v[126:129], v[2:17]
	v_max3_f32 v1, v1, v78, v79
	v_max3_f32 v1, v1, v80, v81
	v_mov_b32_e32 v98, v1
	s_nop 1
	v_permlane32_swap_b32_e32 v1, v98
	v_max_f32_e32 v98, v98, v98
	v_max_f32_e32 v1, v1, v1
	v_max_f32_e32 v1, v1, v98
	v_max_f32_e32 v99, v166, v166
	v_sub_f32_e32 v98, v1, v166
	v_max_f32_e32 v1, v99, v1
	v_mfma_f32_32x32x16_bf16 v[2:17], v[102:105], v[134:137], v[2:17]
	v_sub_f32_e32 v99, v166, v1
	s_mov_b32 s2, 0x42b504f3
	v_mul_f32_e32 v99, 0x3e0293ee, v99
	v_exp_f32_e32 v99, v99
	v_cmp_ge_f32_e32 vcc, s2, v98
	s_cmp_eq_u64 vcc, exec
	s_cselect_b64 vcc, -1, 0
	v_cndmask_b32_e32 v1, v1, v166, vcc
	v_cndmask_b32_e64 v98, v99, 1.0, vcc
	v_mul_f32_e32 v99, 0xbe0293ee, v1
	v_fmamk_f32 v82, v82, 0x3e0293ee, v99
	v_fmamk_f32 v83, v83, 0x3e0293ee, v99
	v_fmamk_f32 v84, v84, 0x3e0293ee, v99
	v_fmamk_f32 v85, v85, 0x3e0293ee, v99
	v_fmamk_f32 v86, v86, 0x3e0293ee, v99
	v_fmamk_f32 v87, v87, 0x3e0293ee, v99
	v_fmamk_f32 v88, v88, 0x3e0293ee, v99
	v_fmamk_f32 v89, v89, 0x3e0293ee, v99
	v_fmamk_f32 v90, v90, 0x3e0293ee, v99
	v_fmamk_f32 v91, v91, 0x3e0293ee, v99
	v_fmamk_f32 v92, v92, 0x3e0293ee, v99
	v_fmamk_f32 v93, v93, 0x3e0293ee, v99
	v_fmamk_f32 v94, v94, 0x3e0293ee, v99
	v_fmamk_f32 v95, v95, 0x3e0293ee, v99
	v_fmamk_f32 v96, v96, 0x3e0293ee, v99
	v_fmamk_f32 v97, v97, 0x3e0293ee, v99
	v_cmp_gt_f32_e32 vcc, 1.0, v98
	s_barrier
	s_cbranch_vccz .LBB0_1157
	s_and_saveexec_b64 s[2:3], s[0:1]
	ds_write_b32 v197, v98 offset:128
	s_or_b64 exec, exec, s[2:3]
	s_waitcnt lgkmcnt(0)
	v_add_u32_e32 v1, v196, v182
	ds_read_b128 v[100:103], v1 offset:224
	ds_read_b128 v[104:107], v1 offset:192
	ds_read_b128 v[112:115], v1 offset:160
	ds_read_b128 v[116:119], v1 offset:128
	s_waitcnt lgkmcnt(3)
	v_pk_mul_f32 v[30:31], v[30:31], v[100:101]
	s_waitcnt lgkmcnt(2)
	v_pk_mul_f32 v[26:27], v[26:27], v[104:105]
	s_waitcnt lgkmcnt(1)
	v_pk_mul_f32 v[22:23], v[22:23], v[112:113]
	v_pk_mul_f32 v[32:33], v[32:33], v[102:103]
	v_pk_mul_f32 v[28:29], v[28:29], v[106:107]
	v_pk_mul_f32 v[24:25], v[24:25], v[114:115]
	s_waitcnt lgkmcnt(0)
	v_pk_mul_f32 v[20:21], v[20:21], v[118:119]
	v_pk_mul_f32 v[18:19], v[18:19], v[116:117]
	v_pk_mul_f32 v[62:63], v[62:63], v[100:101]
	v_pk_mul_f32 v[58:59], v[58:59], v[104:105]
	v_pk_mul_f32 v[54:55], v[54:55], v[112:113]
	v_pk_mul_f32 v[64:65], v[64:65], v[102:103]
	v_pk_mul_f32 v[60:61], v[60:61], v[106:107]
	v_pk_mul_f32 v[56:57], v[56:57], v[114:115]
	v_pk_mul_f32 v[52:53], v[52:53], v[118:119]
	v_pk_mul_f32 v[50:51], v[50:51], v[116:117]
	v_pk_mul_f32 v[46:47], v[46:47], v[100:101]
	v_pk_mul_f32 v[42:43], v[42:43], v[104:105]
	v_pk_mul_f32 v[38:39], v[38:39], v[112:113]
	v_pk_mul_f32 v[48:49], v[48:49], v[102:103]
	v_pk_mul_f32 v[44:45], v[44:45], v[106:107]
	v_pk_mul_f32 v[40:41], v[40:41], v[114:115]
	v_pk_mul_f32 v[36:37], v[36:37], v[118:119]
	v_pk_mul_f32 v[34:35], v[34:35], v[116:117]
	v_pk_mul_f32 v[14:15], v[14:15], v[100:101]
	v_pk_mul_f32 v[10:11], v[10:11], v[104:105]
	v_pk_mul_f32 v[6:7], v[6:7], v[112:113]
	v_pk_mul_f32 v[16:17], v[16:17], v[102:103]
	v_pk_mul_f32 v[12:13], v[12:13], v[106:107]
	v_pk_mul_f32 v[8:9], v[8:9], v[114:115]
	v_pk_mul_f32 v[4:5], v[4:5], v[118:119]
	v_pk_mul_f32 v[2:3], v[2:3], v[116:117]
.LBB0_1157:
	v_exp_f32_e32 v100, v82
	v_exp_f32_e32 v101, v83
	v_exp_f32_e32 v82, v84
	v_fmamk_f32 v66, v66, 0x3e0293ee, v99
	v_exp_f32_e32 v84, v85
	v_fmamk_f32 v113, v77, 0x3e0293ee, v99
	v_exp_f32_e32 v77, v86
	v_exp_f32_e32 v1, v66
	v_add_f32_e32 v66, 0, v100
	v_exp_f32_e32 v83, v87
	v_add_f32_e32 v66, v101, v66
	v_fmamk_f32 v112, v76, 0x3e0293ee, v99
	v_exp_f32_e32 v76, v88
	v_add_f32_e32 v66, v82, v66
	v_fmamk_f32 v114, v78, 0x3e0293ee, v99
	v_exp_f32_e32 v78, v89
	v_add_f32_e32 v66, v84, v66
	v_fmamk_f32 v107, v73, 0x3e0293ee, v99
	v_exp_f32_e32 v73, v90
	v_add_f32_e32 v66, v77, v66
	v_fmamk_f32 v109, v75, 0x3e0293ee, v99
	v_exp_f32_e32 v75, v91
	v_add_f32_e32 v66, v83, v66
	v_fmamk_f32 v105, v71, 0x3e0293ee, v99
	v_exp_f32_e32 v71, v92
	v_add_f32_e32 v66, v76, v66
	v_fmamk_f32 v108, v74, 0x3e0293ee, v99
	v_exp_f32_e32 v74, v93
	v_add_f32_e32 v66, v78, v66
	v_fmamk_f32 v103, v69, 0x3e0293ee, v99
	v_exp_f32_e32 v69, v94
	v_add_f32_e32 v66, v73, v66
	v_fmamk_f32 v106, v72, 0x3e0293ee, v99
	v_exp_f32_e32 v72, v95
	v_add_f32_e32 v66, v75, v66
	v_fmamk_f32 v102, v68, 0x3e0293ee, v99
	v_exp_f32_e32 v68, v96
	v_add_f32_e32 v66, v71, v66
	v_fmamk_f32 v104, v70, 0x3e0293ee, v99
	v_exp_f32_e32 v70, v97
	v_add_f32_e32 v66, v74, v66
	v_fmamk_f32 v67, v67, 0x3e0293ee, v99
	v_add_f32_e32 v66, v69, v66
	v_exp_f32_e32 v85, v67
	v_add_f32_e32 v66, v72, v66
	v_exp_f32_e32 v86, v102
	v_add_f32_e32 v66, v68, v66
	v_exp_f32_e32 v87, v103
	v_add_f32_e32 v66, v70, v66
	v_exp_f32_e32 v88, v104
	v_add_f32_e32 v66, v1, v66
	v_exp_f32_e32 v89, v105
	v_add_f32_e32 v66, v85, v66
	v_exp_f32_e32 v90, v106
	v_add_f32_e32 v66, v86, v66
	v_exp_f32_e32 v91, v107
	v_add_f32_e32 v66, v87, v66
	v_exp_f32_e32 v92, v108
	v_add_f32_e32 v66, v88, v66
	v_exp_f32_e32 v93, v109
	v_add_f32_e32 v66, v89, v66
	v_exp_f32_e32 v94, v112
	v_add_f32_e32 v66, v90, v66
	v_exp_f32_e32 v95, v113
	v_add_f32_e32 v66, v91, v66
	v_fmamk_f32 v79, v79, 0x3e0293ee, v99
	v_exp_f32_e32 v96, v114
	v_add_f32_e32 v66, v92, v66
	v_fmamk_f32 v80, v80, 0x3e0293ee, v99
	v_exp_f32_e32 v97, v79
	v_add_f32_e32 v66, v93, v66
	v_fmac_f32_e32 v99, 0x3e0293ee, v81
	v_exp_f32_e32 v102, v80
	v_add_f32_e32 v66, v94, v66
	v_exp_f32_e32 v99, v99
	v_add_f32_e32 v66, v95, v66
	v_add_f32_e32 v66, v96, v66
	v_add_f32_e32 v66, v97, v66
	v_add_f32_e32 v66, v102, v66
	v_add_f32_e32 v66, v99, v66
	v_mov_b32_e32 v67, v66
	s_nop 1
	v_permlane32_swap_b32_e32 v66, v67
	v_cvt_pk_bf16_f32 v80, v100, v101
	v_cvt_pk_bf16_f32 v81, v82, v84
	v_cvt_pk_bf16_f32 v82, v77, v83
	v_cvt_pk_bf16_f32 v83, v76, v78
	v_cvt_pk_bf16_f32 v76, v73, v75
	v_cvt_pk_bf16_f32 v77, v71, v74
	v_cvt_pk_bf16_f32 v78, v69, v72
	v_cvt_pk_bf16_f32 v79, v68, v70
	v_cvt_pk_bf16_f32 v68, v1, v85
	v_cvt_pk_bf16_f32 v69, v86, v87
	v_cvt_pk_bf16_f32 v70, v88, v89
	v_cvt_pk_bf16_f32 v71, v90, v91
	v_cvt_pk_bf16_f32 v72, v92, v93
	v_cvt_pk_bf16_f32 v73, v94, v95
	v_cvt_pk_bf16_f32 v74, v96, v97
	v_cvt_pk_bf16_f32 v75, v102, v99
	s_nop 0
	v_permlane32_swap_b32_e32 v80, v82
	v_permlane32_swap_b32_e32 v81, v83
	v_permlane32_swap_b32_e32 v76, v78
	v_permlane32_swap_b32_e32 v77, v79
	v_permlane32_swap_b32_e32 v68, v70
	v_permlane32_swap_b32_e32 v69, v71
	v_permlane32_swap_b32_e32 v72, v74
	v_permlane32_swap_b32_e32 v73, v75
	ds_read_b64_tr_b16 v[84:85], v198 offset:0
	ds_read_b64_tr_b16 v[86:87], v198 offset:0x800
	ds_read_b64_tr_b16 v[88:89], v198 offset:0x1000
	ds_read_b64_tr_b16 v[90:91], v198 offset:0x1800
	ds_read_b64_tr_b16 v[92:93], v198 offset:0x2000
	ds_read_b64_tr_b16 v[94:95], v198 offset:0x2800
	ds_read_b64_tr_b16 v[100:101], v198 offset:0x3000
	ds_read_b64_tr_b16 v[102:103], v198 offset:0x3800
	s_waitcnt lgkmcnt(0)
	s_nop 0
	v_mfma_f32_32x32x16_bf16 v[18:33], v[80:83], v[84:87], v[18:33]
	ds_read_b64_tr_b16 v[84:85], v198 offset:0x200
	ds_read_b64_tr_b16 v[86:87], v198 offset:0xa00
	v_mfma_f32_32x32x16_bf16 v[18:33], v[76:79], v[88:91], v[18:33]
	ds_read_b64_tr_b16 v[88:89], v198 offset:0x1200
	ds_read_b64_tr_b16 v[90:91], v198 offset:0x1a00
	v_mfma_f32_32x32x16_bf16 v[18:33], v[68:71], v[92:95], v[18:33]
	ds_read_b64_tr_b16 v[92:93], v198 offset:0x2200
	ds_read_b64_tr_b16 v[94:95], v198 offset:0x2a00
	ds_read_b64_tr_b16 v[104:105], v198 offset:0x3200
	ds_read_b64_tr_b16 v[106:107], v198 offset:0x3a00
	v_mfma_f32_32x32x16_bf16 v[18:33], v[72:75], v[100:103], v[18:33]
	s_waitcnt lgkmcnt(0)
	v_mfma_f32_32x32x16_bf16 v[50:65], v[80:83], v[84:87], v[50:65]
	ds_read_b64_tr_b16 v[84:85], v198 offset:0x400
	ds_read_b64_tr_b16 v[86:87], v198 offset:0xc00
	v_mfma_f32_32x32x16_bf16 v[50:65], v[76:79], v[88:91], v[50:65]
	ds_read_b64_tr_b16 v[88:89], v198 offset:0x1400
	ds_read_b64_tr_b16 v[90:91], v198 offset:0x1c00
	v_mfma_f32_32x32x16_bf16 v[50:65], v[68:71], v[92:95], v[50:65]
	ds_read_b64_tr_b16 v[92:93], v198 offset:0x2400
	ds_read_b64_tr_b16 v[94:95], v198 offset:0x2c00
	ds_read_b64_tr_b16 v[100:101], v198 offset:0x3400
	ds_read_b64_tr_b16 v[102:103], v198 offset:0x3c00
	v_mfma_f32_32x32x16_bf16 v[50:65], v[72:75], v[104:107], v[50:65]
	s_waitcnt lgkmcnt(0)
	v_mfma_f32_32x32x16_bf16 v[34:49], v[80:83], v[84:87], v[34:49]
	ds_read_b64_tr_b16 v[84:85], v198 offset:0x600
	ds_read_b64_tr_b16 v[86:87], v198 offset:0xe00
	v_mfma_f32_32x32x16_bf16 v[34:49], v[76:79], v[88:91], v[34:49]
	ds_read_b64_tr_b16 v[88:89], v198 offset:0x1600
	ds_read_b64_tr_b16 v[90:91], v198 offset:0x1e00
	v_mfma_f32_32x32x16_bf16 v[34:49], v[68:71], v[92:95], v[34:49]
	ds_read_b64_tr_b16 v[92:93], v198 offset:0x2600
	ds_read_b64_tr_b16 v[94:95], v198 offset:0x2e00
	ds_read_b64_tr_b16 v[104:105], v198 offset:0x3600
	ds_read_b64_tr_b16 v[106:107], v198 offset:0x3e00
	v_mfma_f32_32x32x16_bf16 v[34:49], v[72:75], v[100:103], v[34:49]
	s_waitcnt lgkmcnt(0)
	v_mfma_f32_32x32x16_bf16 v[2:17], v[80:83], v[84:87], v[2:17]
	v_mfma_f32_32x32x16_bf16 v[2:17], v[76:79], v[88:91], v[2:17]
	v_mfma_f32_32x32x16_bf16 v[2:17], v[68:71], v[92:95], v[2:17]
	v_mfma_f32_32x32x16_bf16 v[2:17], v[72:75], v[104:107], v[2:17]
	s_and_saveexec_b64 s[2:3], s[0:1]
	v_add_f32_e32 v1, v110, v111
	v_fmac_f32_e32 v1, v183, v162
	v_add_f32_e32 v66, v66, v67
	v_fmac_f32_e32 v66, v1, v98
	ds_write_b32 v197, v66
	s_or_b64 exec, exec, s[2:3]
	s_waitcnt lgkmcnt(0)
	v_add_u32_e32 v1, v196, v182
	ds_read_b128 v[66:69], v1
	ds_read_b128 v[70:73], v1 offset:32
	s_add_u32 s0, s4, s10
	s_addc_u32 s1, s5, s11
	s_add_i32 s2, 0, 0x10800
	s_waitcnt lgkmcnt(1)
	v_rcp_f32_e32 v74, v66
	v_rcp_f32_e32 v75, v67
	v_rcp_f32_e32 v76, v68
	v_rcp_f32_e32 v77, v69
	s_waitcnt lgkmcnt(0)
	v_rcp_f32_e32 v78, v70
	ds_read_b128 v[66:69], v1 offset:64
	v_rcp_f32_e32 v79, v71
	v_rcp_f32_e32 v80, v72
	v_rcp_f32_e32 v81, v73
	ds_read_b128 v[70:73], v1 offset:96
	s_waitcnt lgkmcnt(1)
	v_rcp_f32_e32 v1, v66
	v_rcp_f32_e32 v66, v67
	v_rcp_f32_e32 v67, v68
	v_rcp_f32_e32 v68, v69
	s_waitcnt lgkmcnt(0)
	v_rcp_f32_e32 v69, v70
	v_rcp_f32_e32 v70, v71
	v_rcp_f32_e32 v71, v72
	v_rcp_f32_e32 v72, v73
	v_lshl_add_u32 v73, v181, 13, s2
	v_mul_f32_e32 v18, v18, v74
	s_mov_b32 s2, 0xc3e00000
	v_mov_b32_e32 v83, 0x43e00000
	v_mul_f32_e32 v19, v19, v75
	v_med3_f32 v18, v18, s2, v83
	v_med3_f32 v19, v19, s2, v83
	v_mov_b32_e32 v84, 0
	v_cvt_pk_fp8_f32 v84, v18, v19
	v_mul_f32_e32 v18, v20, v76
	v_mul_f32_e32 v19, v21, v77
	v_med3_f32 v18, v18, s2, v83
	v_med3_f32 v19, v19, s2, v83
	v_mov_b32_e32 v20, 0
	v_cvt_pk_fp8_f32 v20, v18, v19
	v_lshlrev_b32_e32 v82, 9, v193
	v_add3_u32 v82, v73, v82, v179
	v_lshrrev_b32_e32 v18, 8, v84
	ds_write_b8 v82, v84
	ds_write_b8 v82, v18 offset:128
	ds_write_b8 v82, v20 offset:256
	v_lshrrev_b32_e32 v18, 8, v20
	ds_write_b8 v82, v18 offset:384
	v_mul_f32_e32 v18, v22, v78
	v_mul_f32_e32 v19, v23, v79
	v_med3_f32 v18, v18, s2, v83
	v_med3_f32 v19, v19, s2, v83
	v_mov_b32_e32 v20, 0
	v_cvt_pk_fp8_f32 v20, v18, v19
	v_mul_f32_e32 v18, v24, v80
	v_mul_f32_e32 v19, v25, v81
	v_med3_f32 v18, v18, s2, v83
	v_med3_f32 v19, v19, s2, v83
	v_mov_b32_e32 v21, 0
	v_cvt_pk_fp8_f32 v21, v18, v19
	v_lshrrev_b32_e32 v18, 8, v20
	ds_write_b8 v82, v20 offset:1024
	ds_write_b8 v82, v18 offset:1152
	ds_write_b8 v82, v21 offset:1280
	v_lshrrev_b32_e32 v18, 8, v21
	ds_write_b8 v82, v18 offset:1408
	v_mul_f32_e32 v18, v26, v1
	v_mul_f32_e32 v19, v27, v66
	v_med3_f32 v18, v18, s2, v83
	v_med3_f32 v19, v19, s2, v83
	v_mov_b32_e32 v20, 0
	v_cvt_pk_fp8_f32 v20, v18, v19
	v_mul_f32_e32 v18, v28, v67
	v_mul_f32_e32 v19, v29, v68
	v_med3_f32 v18, v18, s2, v83
	v_med3_f32 v19, v19, s2, v83
	v_mov_b32_e32 v21, 0
	v_cvt_pk_fp8_f32 v21, v18, v19
	v_lshrrev_b32_e32 v18, 8, v20
	ds_write_b8 v82, v20 offset:2048
	ds_write_b8 v82, v18 offset:2176
	ds_write_b8 v82, v21 offset:2304
	v_lshrrev_b32_e32 v18, 8, v21
	ds_write_b8 v82, v18 offset:2432
	v_mul_f32_e32 v18, v30, v69
	v_mul_f32_e32 v19, v31, v70
	v_med3_f32 v18, v18, s2, v83
	v_med3_f32 v19, v19, s2, v83
	v_mov_b32_e32 v20, 0
	v_cvt_pk_fp8_f32 v20, v18, v19
	v_mul_f32_e32 v18, v32, v71
	v_mul_f32_e32 v19, v33, v72
	v_med3_f32 v18, v18, s2, v83
	v_med3_f32 v19, v19, s2, v83
	v_mov_b32_e32 v21, 0
	v_cvt_pk_fp8_f32 v21, v18, v19
	v_lshrrev_b32_e32 v18, 8, v20
	ds_write_b8 v82, v20 offset:3072
	ds_write_b8 v82, v18 offset:3200
	ds_write_b8 v82, v21 offset:3328
	v_lshrrev_b32_e32 v18, 8, v21
	ds_write_b8 v82, v18 offset:3456
	v_mul_f32_e32 v18, v50, v74
	v_mul_f32_e32 v19, v51, v75
	v_med3_f32 v18, v18, s2, v83
	v_med3_f32 v19, v19, s2, v83
	v_mov_b32_e32 v20, 0
	v_cvt_pk_fp8_f32 v20, v18, v19
	v_mul_f32_e32 v18, v52, v76
	v_mul_f32_e32 v19, v53, v77
	v_med3_f32 v18, v18, s2, v83
	v_med3_f32 v19, v19, s2, v83
	v_mov_b32_e32 v21, 0
	v_cvt_pk_fp8_f32 v21, v18, v19
	v_lshrrev_b32_e32 v18, 8, v20
	ds_write_b8 v82, v20 offset:32
	ds_write_b8 v82, v18 offset:160
	ds_write_b8 v82, v21 offset:288
	v_lshrrev_b32_e32 v18, 8, v21
	ds_write_b8 v82, v18 offset:416
	v_mul_f32_e32 v18, v54, v78
	v_mul_f32_e32 v19, v55, v79
	v_med3_f32 v18, v18, s2, v83
	v_med3_f32 v19, v19, s2, v83
	v_mov_b32_e32 v20, 0
	v_cvt_pk_fp8_f32 v20, v18, v19
	v_mul_f32_e32 v18, v56, v80
	v_mul_f32_e32 v19, v57, v81
	v_med3_f32 v18, v18, s2, v83
	v_med3_f32 v19, v19, s2, v83
	v_mov_b32_e32 v21, 0
	v_cvt_pk_fp8_f32 v21, v18, v19
	v_lshrrev_b32_e32 v18, 8, v20
	ds_write_b8 v82, v20 offset:1056
	ds_write_b8 v82, v18 offset:1184
	ds_write_b8 v82, v21 offset:1312
	v_lshrrev_b32_e32 v18, 8, v21
	ds_write_b8 v82, v18 offset:1440
	v_mul_f32_e32 v18, v58, v1
	v_mul_f32_e32 v19, v59, v66
	v_med3_f32 v18, v18, s2, v83
	v_med3_f32 v19, v19, s2, v83
	v_mov_b32_e32 v20, 0
	v_cvt_pk_fp8_f32 v20, v18, v19
	v_mul_f32_e32 v18, v60, v67
	v_mul_f32_e32 v19, v61, v68
	v_med3_f32 v18, v18, s2, v83
	v_med3_f32 v19, v19, s2, v83
	v_mov_b32_e32 v21, 0
	v_cvt_pk_fp8_f32 v21, v18, v19
	v_lshrrev_b32_e32 v18, 8, v20
	ds_write_b8 v82, v20 offset:2080
	ds_write_b8 v82, v18 offset:2208
	ds_write_b8 v82, v21 offset:2336
	v_lshrrev_b32_e32 v18, 8, v21
	ds_write_b8 v82, v18 offset:2464
	v_mul_f32_e32 v18, v62, v69
	v_mul_f32_e32 v19, v63, v70
	v_med3_f32 v18, v18, s2, v83
	v_med3_f32 v19, v19, s2, v83
	v_mov_b32_e32 v20, 0
	v_cvt_pk_fp8_f32 v20, v18, v19
	v_mul_f32_e32 v18, v64, v71
	v_mul_f32_e32 v19, v65, v72
	v_med3_f32 v18, v18, s2, v83
	v_med3_f32 v19, v19, s2, v83
	v_mov_b32_e32 v21, 0
	v_cvt_pk_fp8_f32 v21, v18, v19
	v_lshrrev_b32_e32 v18, 8, v20
	ds_write_b8 v82, v20 offset:3104
	ds_write_b8 v82, v18 offset:3232
	ds_write_b8 v82, v21 offset:3360
	v_lshrrev_b32_e32 v18, 8, v21
	ds_write_b8 v82, v18 offset:3488
	v_mul_f32_e32 v18, v34, v74
	v_mul_f32_e32 v19, v35, v75
	v_med3_f32 v18, v18, s2, v83
	v_med3_f32 v19, v19, s2, v83
	v_mov_b32_e32 v20, 0
	v_cvt_pk_fp8_f32 v20, v18, v19
	v_mul_f32_e32 v18, v36, v76
	v_mul_f32_e32 v19, v37, v77
	v_med3_f32 v18, v18, s2, v83
	v_med3_f32 v19, v19, s2, v83
	v_mov_b32_e32 v21, 0
	v_cvt_pk_fp8_f32 v21, v18, v19
	v_lshrrev_b32_e32 v18, 8, v20
	ds_write_b8 v82, v20 offset:64
	ds_write_b8 v82, v18 offset:192
	ds_write_b8 v82, v21 offset:320
	v_lshrrev_b32_e32 v18, 8, v21
	ds_write_b8 v82, v18 offset:448
	v_mul_f32_e32 v18, v38, v78
	v_mul_f32_e32 v19, v39, v79
	v_med3_f32 v18, v18, s2, v83
	v_med3_f32 v19, v19, s2, v83
	v_mov_b32_e32 v20, 0
	v_cvt_pk_fp8_f32 v20, v18, v19
	v_mul_f32_e32 v18, v40, v80
	v_mul_f32_e32 v19, v41, v81
	v_med3_f32 v18, v18, s2, v83
	v_med3_f32 v19, v19, s2, v83
	v_mov_b32_e32 v21, 0
	v_cvt_pk_fp8_f32 v21, v18, v19
	v_lshrrev_b32_e32 v18, 8, v20
	ds_write_b8 v82, v20 offset:1088
	ds_write_b8 v82, v18 offset:1216
	ds_write_b8 v82, v21 offset:1344
	v_lshrrev_b32_e32 v18, 8, v21
	ds_write_b8 v82, v18 offset:1472
	v_mul_f32_e32 v18, v42, v1
	v_mul_f32_e32 v19, v43, v66
	v_med3_f32 v18, v18, s2, v83
	v_med3_f32 v19, v19, s2, v83
	v_mov_b32_e32 v20, 0
	v_cvt_pk_fp8_f32 v20, v18, v19
	v_mul_f32_e32 v18, v44, v67
	v_mul_f32_e32 v19, v45, v68
	v_med3_f32 v18, v18, s2, v83
	v_med3_f32 v19, v19, s2, v83
	v_mov_b32_e32 v21, 0
	v_cvt_pk_fp8_f32 v21, v18, v19
	v_lshrrev_b32_e32 v18, 8, v20
	ds_write_b8 v82, v20 offset:2112
	ds_write_b8 v82, v18 offset:2240
	ds_write_b8 v82, v21 offset:2368
	v_lshrrev_b32_e32 v18, 8, v21
	ds_write_b8 v82, v18 offset:2496
	v_mul_f32_e32 v18, v46, v69
	v_mul_f32_e32 v19, v47, v70
	v_med3_f32 v18, v18, s2, v83
	v_med3_f32 v19, v19, s2, v83
	v_mov_b32_e32 v20, 0
	v_cvt_pk_fp8_f32 v20, v18, v19
	v_mul_f32_e32 v18, v48, v71
	v_mul_f32_e32 v19, v49, v72
	v_med3_f32 v18, v18, s2, v83
	v_med3_f32 v19, v19, s2, v83
	v_mov_b32_e32 v21, 0
	v_cvt_pk_fp8_f32 v21, v18, v19
	v_lshrrev_b32_e32 v18, 8, v20
	ds_write_b8 v82, v20 offset:3136
	ds_write_b8 v82, v18 offset:3264
	ds_write_b8 v82, v21 offset:3392
	v_lshrrev_b32_e32 v18, 8, v21
	v_mul_f32_e32 v2, v2, v74
	v_mul_f32_e32 v3, v3, v75
	ds_write_b8 v82, v18 offset:3520
	v_med3_f32 v2, v2, s2, v83
	v_med3_f32 v3, v3, s2, v83
	v_mov_b32_e32 v18, 0
	v_cvt_pk_fp8_f32 v18, v2, v3
	v_mul_f32_e32 v2, v4, v76
	v_mul_f32_e32 v3, v5, v77
	v_med3_f32 v2, v2, s2, v83
	v_med3_f32 v3, v3, s2, v83
	v_mov_b32_e32 v4, 0
	v_cvt_pk_fp8_f32 v4, v2, v3
	v_lshrrev_b32_e32 v2, 8, v18
	ds_write_b8 v82, v18 offset:96
	ds_write_b8 v82, v2 offset:224
	ds_write_b8 v82, v4 offset:352
	v_lshrrev_b32_e32 v2, 8, v4
	ds_write_b8 v82, v2 offset:480
	v_mul_f32_e32 v2, v6, v78
	v_mul_f32_e32 v3, v7, v79
	v_med3_f32 v2, v2, s2, v83
	v_med3_f32 v3, v3, s2, v83
	v_mov_b32_e32 v4, 0
	v_cvt_pk_fp8_f32 v4, v2, v3
	v_mul_f32_e32 v2, v8, v80
	v_mul_f32_e32 v3, v9, v81
	v_med3_f32 v2, v2, s2, v83
	v_med3_f32 v3, v3, s2, v83
	v_mov_b32_e32 v5, 0
	v_cvt_pk_fp8_f32 v5, v2, v3
	v_lshrrev_b32_e32 v2, 8, v4
	ds_write_b8 v82, v4 offset:1120
	ds_write_b8 v82, v2 offset:1248
	ds_write_b8 v82, v5 offset:1376
	v_lshrrev_b32_e32 v2, 8, v5
	ds_write_b8 v82, v2 offset:1504
	v_mul_f32_e32 v1, v10, v1
	v_mul_f32_e32 v2, v11, v66
	v_med3_f32 v1, v1, s2, v83
	v_med3_f32 v2, v2, s2, v83
	v_mov_b32_e32 v3, 0
	v_cvt_pk_fp8_f32 v3, v1, v2
	v_mul_f32_e32 v1, v12, v67
	v_mul_f32_e32 v2, v13, v68
	v_med3_f32 v1, v1, s2, v83
	v_med3_f32 v2, v2, s2, v83
	v_mov_b32_e32 v4, 0
	v_cvt_pk_fp8_f32 v4, v1, v2
	v_lshrrev_b32_e32 v1, 8, v3
	ds_write_b8 v82, v3 offset:2144
	ds_write_b8 v82, v1 offset:2272
	ds_write_b8 v82, v4 offset:2400
	v_lshrrev_b32_e32 v1, 8, v4
	ds_write_b8 v82, v1 offset:2528
	v_mul_f32_e32 v1, v14, v69
	v_mul_f32_e32 v2, v15, v70
	v_med3_f32 v1, v1, s2, v83
	v_med3_f32 v2, v2, s2, v83
	v_mov_b32_e32 v3, 0
	v_cvt_pk_fp8_f32 v3, v1, v2
	v_mul_f32_e32 v1, v16, v71
	v_mul_f32_e32 v2, v17, v72
	v_med3_f32 v1, v1, s2, v83
	v_med3_f32 v2, v2, s2, v83
	v_mov_b32_e32 v4, 0
	v_cvt_pk_fp8_f32 v4, v1, v2
	v_lshrrev_b32_e32 v1, 8, v3
	ds_write_b8 v82, v3 offset:3168
	ds_write_b8 v82, v1 offset:3296
	ds_write_b8 v82, v4 offset:3424
	v_lshrrev_b32_e32 v1, 8, v4
	ds_write_b8 v82, v1 offset:3552
	v_lshrrev_b32_e32 v1, 3, v254
	v_lshlrev_b32_e32 v2, 7, v1
	v_mov_b32_e32 v181, 0
	s_waitcnt lgkmcnt(0)
	v_add3_u32 v14, v73, v2, v178
	v_lshl_add_u64 v[6:7], s[0:1], 0, v[180:181]
	v_lshlrev_b32_e32 v180, 11, v1
	ds_read_b128 v[2:5], v14
	v_lshl_add_u64 v[6:7], v[6:7], 0, v[180:181]
	v_mov_b32_e32 v179, v181
	v_lshl_add_u64 v[10:11], v[6:7], 0, v[178:179]
	ds_read_b128 v[6:9], v14 offset:1024
	s_movk_i32 s0, 0x4000
	s_waitcnt lgkmcnt(1)
	global_store_dwordx4 v[10:11], v[2:5], off
	s_nop 1
	v_add_co_u32_e32 v2, vcc, s0, v10
	s_nop 1
	v_addc_co_u32_e32 v3, vcc, 0, v11, vcc
	s_waitcnt lgkmcnt(0)
	global_store_dwordx4 v[2:3], v[6:9], off
	ds_read_b128 v[2:5], v14 offset:2048
	ds_read_b128 v[6:9], v14 offset:3072
	v_add_co_u32_e32 v12, vcc, 0x8000, v10
	s_nop 1
	v_addc_co_u32_e32 v13, vcc, 0, v11, vcc
	s_waitcnt lgkmcnt(1)
	global_store_dwordx4 v[12:13], v[2:5], off
	s_nop 1
	v_add_co_u32_e32 v2, vcc, 0xc000, v10
	s_nop 1
	v_addc_co_u32_e32 v3, vcc, 0, v11, vcc
	s_waitcnt lgkmcnt(0)
	global_store_dwordx4 v[2:3], v[6:9], off
	s_waitcnt lgkmcnt(0)
	s_barrier
	s_cmp_lg_u32 s72, 1
	s_cbranch_scc1 .LBB0_1138

.LBB0_1180:
	ds_read_b128 v[66:69], v205 offset:49152
	ds_read_b128 v[70:73], v205 offset:57344
	ds_read_b128 v[222:225], v206 offset:49152
	ds_read_b128 v[226:229], v206 offset:57344
	v_exp_f32_e32 v1, v156
	v_exp_f32_e32 v156, v157
	s_waitcnt lgkmcnt(3)
	v_mfma_f32_32x32x16_bf16 v[82:97], v[66:69], v[126:129], 0
	v_exp_f32_e32 v157, v160
	v_exp_f32_e32 v160, v161
	v_add_f32_e32 v161, 0, v177
	v_add_f32_e32 v161, v220, v161
	v_add_f32_e32 v161, v163, v161
	v_add_f32_e32 v161, v217, v161
	v_add_f32_e32 v161, v164, v161
	s_waitcnt lgkmcnt(2)
	v_mfma_f32_32x32x16_bf16 v[66:81], v[70:73], v[126:129], 0
	v_add_f32_e32 v161, v176, v161
	v_add_f32_e32 v161, v165, v161
	v_add_f32_e32 v161, v175, v161
	v_add_f32_e32 v161, v172, v161
	v_add_f32_e32 v161, v174, v161
	v_add_f32_e32 v161, v171, v161
	v_add_f32_e32 v161, v173, v161
	s_waitcnt lgkmcnt(1)
	v_mfma_f32_32x32x16_bf16 v[82:97], v[222:225], v[114:117], v[82:97]
	v_add_f32_e32 v161, v168, v161
	v_add_f32_e32 v161, v170, v161
	v_exp_f32_e32 v154, v154
	v_add_f32_e32 v161, v167, v161
	v_exp_f32_e32 v155, v155
	v_add_f32_e32 v161, v169, v161
	v_exp_f32_e32 v150, v150
	s_waitcnt lgkmcnt(0)
	v_mfma_f32_32x32x16_bf16 v[66:81], v[226:229], v[114:117], v[66:81]
	ds_read_b128 v[222:225], v207 offset:49152
	ds_read_b128 v[226:229], v207 offset:57344
	v_add_f32_e32 v161, v1, v161
	v_exp_f32_e32 v151, v151
	v_add_f32_e32 v161, v156, v161
	v_exp_f32_e32 v148, v148
	v_add_f32_e32 v161, v154, v161
	v_exp_f32_e32 v149, v149
	s_waitcnt lgkmcnt(1)
	v_mfma_f32_32x32x16_bf16 v[82:97], v[222:225], v[118:121], v[82:97]
	v_add_f32_e32 v161, v155, v161
	v_exp_f32_e32 v146, v146
	v_add_f32_e32 v161, v150, v161
	v_exp_f32_e32 v147, v147
	v_add_f32_e32 v161, v151, v161
	v_add_f32_e32 v161, v148, v161
	v_add_f32_e32 v161, v149, v161
	s_waitcnt lgkmcnt(0)
	v_mfma_f32_32x32x16_bf16 v[66:81], v[226:229], v[118:121], v[66:81]
	ds_read_b128 v[222:225], v208 offset:49152
	ds_read_b128 v[226:229], v208 offset:57344
	v_exp_f32_e32 v158, v158
	v_add_f32_e32 v161, v146, v161
	v_exp_f32_e32 v159, v159
	v_add_f32_e32 v161, v147, v161
	v_exp_f32_e32 v152, v152
	v_add_f32_e32 v161, v157, v161
	s_waitcnt lgkmcnt(1)
	v_mfma_f32_32x32x16_bf16 v[82:97], v[222:225], v[122:125], v[82:97]
	v_exp_f32_e32 v153, v153
	v_add_f32_e32 v161, v160, v161
	v_add_f32_e32 v161, v158, v161
	v_add_f32_e32 v161, v159, v161
	v_add_f32_e32 v161, v152, v161
	v_add_f32_e32 v214, v153, v161
	v_mov_b32_e32 v215, v214
	s_waitcnt lgkmcnt(0)
	v_mfma_f32_32x32x16_bf16 v[66:81], v[226:229], v[122:125], v[66:81]
	ds_read_b128 v[222:225], v209 offset:49152
	ds_read_b128 v[226:229], v209 offset:57344
	v_permlane32_swap_b32_e32 v214, v215
	s_waitcnt lgkmcnt(1)
	v_mfma_f32_32x32x16_bf16 v[82:97], v[222:225], v[110:113], v[82:97]
	s_waitcnt lgkmcnt(0)
	v_mfma_f32_32x32x16_bf16 v[66:81], v[226:229], v[110:113], v[66:81]
	ds_read_b128 v[222:225], v210 offset:49152
	ds_read_b128 v[226:229], v210 offset:57344
	s_waitcnt lgkmcnt(1)
	v_mfma_f32_32x32x16_bf16 v[82:97], v[222:225], v[106:109], v[82:97]
	s_waitcnt lgkmcnt(0)
	v_mfma_f32_32x32x16_bf16 v[66:81], v[226:229], v[106:109], v[66:81]
	ds_read_b128 v[222:225], v211 offset:49152
	ds_read_b128 v[226:229], v211 offset:57344
	s_waitcnt lgkmcnt(1)
	v_mfma_f32_32x32x16_bf16 v[82:97], v[222:225], v[102:105], v[82:97]
	s_waitcnt lgkmcnt(0)
	v_mfma_f32_32x32x16_bf16 v[66:81], v[226:229], v[102:105], v[66:81]
	ds_read_b128 v[222:225], v212 offset:49152
	ds_read_b128 v[226:229], v212 offset:57344
	v_cvt_pk_bf16_f32 v162, v177, v220
	v_cvt_pk_bf16_f32 v163, v163, v217
	v_cvt_pk_bf16_f32 v164, v164, v176
	v_cvt_pk_bf16_f32 v165, v165, v175
	v_cvt_pk_bf16_f32 v172, v172, v174
	v_cvt_pk_bf16_f32 v173, v171, v173
	s_waitcnt lgkmcnt(1)
	v_mfma_f32_32x32x16_bf16 v[82:97], v[222:225], v[98:101], v[82:97]
	v_cvt_pk_bf16_f32 v174, v168, v170
	v_cvt_pk_bf16_f32 v175, v167, v169
	v_cvt_pk_bf16_f32 v168, v1, v156
	v_cvt_pk_bf16_f32 v169, v154, v155
	v_cvt_pk_bf16_f32 v170, v150, v151
	v_cvt_pk_bf16_f32 v171, v148, v149
	v_cvt_pk_bf16_f32 v216, v146, v147
	s_waitcnt lgkmcnt(0)
	v_mfma_f32_32x32x16_bf16 v[66:81], v[226:229], v[98:101], v[66:81]
	v_cvt_pk_bf16_f32 v217, v157, v160
	v_cvt_pk_bf16_f32 v218, v158, v159
	v_permlane32_swap_b32_e32 v162, v164
	v_cvt_pk_bf16_f32 v219, v152, v153
	v_permlane32_swap_b32_e32 v216, v218
	v_permlane32_swap_b32_e32 v163, v165
	v_permlane32_swap_b32_e32 v172, v174
	v_permlane32_swap_b32_e32 v173, v175
	v_permlane32_swap_b32_e32 v168, v170
	v_permlane32_swap_b32_e32 v169, v171
	v_permlane32_swap_b32_e32 v217, v219
	v_lshl_add_u64 v[154:155], s[16:17], 0, v[188:189]
	v_add_co_u32_e32 v146, vcc, s23, v154
	v_lshl_add_u64 v[156:157], s[16:17], 0, v[190:191]
	s_nop 0
	v_addc_co_u32_e32 v147, vcc, 0, v155, vcc
	v_add_co_u32_e32 v150, vcc, s23, v156
	s_nop 1
	v_addc_co_u32_e32 v151, vcc, 0, v157, vcc
	v_add_co_u32_e32 v154, vcc, s24, v154
	global_load_dwordx4 v[146:149], v[146:147], off
	s_nop 0
	global_load_dwordx4 v[150:153], v[150:151], off
	v_addc_co_u32_e32 v155, vcc, 0, v155, vcc
	v_add_co_u32_e32 v158, vcc, s24, v156
	s_nop 1
	v_addc_co_u32_e32 v159, vcc, 0, v157, vcc
	global_load_dwordx4 v[154:157], v[154:155], off
	s_nop 0
	global_load_dwordx4 v[158:161], v[158:159], off
	ds_read_b64_tr_b16 v[220:221], v199 offset:0
	ds_read_b64_tr_b16 v[222:223], v199 offset:0x800
	ds_read_b64_tr_b16 v[224:225], v199 offset:0x1000
	ds_read_b64_tr_b16 v[226:227], v199 offset:0x1800
	ds_read_b64_tr_b16 v[228:229], v199 offset:0x2000
	ds_read_b64_tr_b16 v[230:231], v199 offset:0x2800
	ds_read_b64_tr_b16 v[232:233], v199 offset:0x3000
	ds_read_b64_tr_b16 v[234:235], v199 offset:0x3800
	s_waitcnt lgkmcnt(0)
	s_nop 0
	v_mfma_f32_32x32x16_bf16 v[18:33], v[162:165], v[220:223], v[18:33]
	ds_read_b64_tr_b16 v[220:221], v199 offset:0x200
	ds_read_b64_tr_b16 v[222:223], v199 offset:0xa00
	v_mfma_f32_32x32x16_bf16 v[18:33], v[172:175], v[224:227], v[18:33]
	ds_read_b64_tr_b16 v[224:225], v199 offset:0x1200
	ds_read_b64_tr_b16 v[226:227], v199 offset:0x1a00
	v_mfma_f32_32x32x16_bf16 v[18:33], v[168:171], v[228:231], v[18:33]
	ds_read_b64_tr_b16 v[228:229], v199 offset:0x2200
	ds_read_b64_tr_b16 v[230:231], v199 offset:0x2a00
	ds_read_b64_tr_b16 v[236:237], v199 offset:0x3200
	ds_read_b64_tr_b16 v[238:239], v199 offset:0x3a00
	v_mfma_f32_32x32x16_bf16 v[18:33], v[216:219], v[232:235], v[18:33]
	s_waitcnt lgkmcnt(0)
	v_mfma_f32_32x32x16_bf16 v[50:65], v[162:165], v[220:223], v[50:65]
	ds_read_b64_tr_b16 v[220:221], v199 offset:0x400
	ds_read_b64_tr_b16 v[222:223], v199 offset:0xc00
	v_mfma_f32_32x32x16_bf16 v[50:65], v[172:175], v[224:227], v[50:65]
	ds_read_b64_tr_b16 v[224:225], v199 offset:0x1400
	ds_read_b64_tr_b16 v[226:227], v199 offset:0x1c00
	v_mfma_f32_32x32x16_bf16 v[50:65], v[168:171], v[228:231], v[50:65]
	ds_read_b64_tr_b16 v[228:229], v199 offset:0x2400
	ds_read_b64_tr_b16 v[230:231], v199 offset:0x2c00
	ds_read_b64_tr_b16 v[232:233], v199 offset:0x3400
	ds_read_b64_tr_b16 v[234:235], v199 offset:0x3c00
	v_mfma_f32_32x32x16_bf16 v[50:65], v[216:219], v[236:239], v[50:65]
	s_waitcnt lgkmcnt(0)
	v_mfma_f32_32x32x16_bf16 v[34:49], v[162:165], v[220:223], v[34:49]
	ds_read_b64_tr_b16 v[220:221], v199 offset:0x600
	ds_read_b64_tr_b16 v[222:223], v199 offset:0xe00
	v_mfma_f32_32x32x16_bf16 v[34:49], v[172:175], v[224:227], v[34:49]
	ds_read_b64_tr_b16 v[224:225], v199 offset:0x1600
	ds_read_b64_tr_b16 v[226:227], v199 offset:0x1e00
	v_mfma_f32_32x32x16_bf16 v[34:49], v[168:171], v[228:231], v[34:49]
	ds_read_b64_tr_b16 v[228:229], v199 offset:0x2600
	ds_read_b64_tr_b16 v[230:231], v199 offset:0x2e00
	ds_read_b64_tr_b16 v[236:237], v199 offset:0x3600
	ds_read_b64_tr_b16 v[238:239], v199 offset:0x3e00
	v_mfma_f32_32x32x16_bf16 v[34:49], v[216:219], v[232:235], v[34:49]
	s_waitcnt lgkmcnt(0)
	v_mfma_f32_32x32x16_bf16 v[2:17], v[162:165], v[220:223], v[2:17]
	v_max_f32_e32 v1, v83, v83
	v_max_f32_e32 v167, v82, v82
	v_max_f32_e32 v1, v167, v1
	v_max3_f32 v1, v1, v84, v85
	v_max3_f32 v1, v1, v86, v87
	v_max3_f32 v1, v1, v88, v89
	v_max3_f32 v1, v1, v90, v91
	v_max3_f32 v1, v1, v92, v93
	v_mfma_f32_32x32x16_bf16 v[2:17], v[172:175], v[224:227], v[2:17]
	v_max3_f32 v1, v1, v94, v95
	v_max3_f32 v1, v1, v96, v97
	v_max3_f32 v1, v1, v66, v67
	v_max3_f32 v1, v1, v68, v69
	v_max3_f32 v1, v1, v70, v71
	v_max3_f32 v1, v1, v72, v73
	v_max3_f32 v1, v1, v74, v75
	v_max3_f32 v1, v1, v76, v77
	v_mfma_f32_32x32x16_bf16 v[2:17], v[168:171], v[228:231], v[2:17]
	v_max3_f32 v1, v1, v78, v79
	v_max3_f32 v1, v1, v80, v81
	v_mov_b32_e32 v162, v1
	s_nop 1
	v_permlane32_swap_b32_e32 v1, v162
	v_max_f32_e32 v162, v162, v162
	v_max_f32_e32 v1, v1, v1
	v_max_f32_e32 v1, v1, v162
	v_max_f32_e32 v162, v166, v166
	v_max_f32_e32 v162, v162, v1
	v_sub_f32_e32 v163, v1, v166
	v_mfma_f32_32x32x16_bf16 v[2:17], v[216:219], v[236:239], v[2:17]
	v_sub_f32_e32 v1, v166, v162
	v_mul_f32_e32 v1, 0x3e0293ee, v1
	v_exp_f32_e32 v1, v1
	v_cmp_ge_f32_e32 vcc, s22, v163
	s_cmp_eq_u64 vcc, exec
	s_cselect_b64 s[2:3], -1, 0
	s_barrier
	s_waitcnt vmcnt(4)
	v_cndmask_b32_e64 v216, v1, 1.0, s[2:3]
	v_cmp_gt_f32_e32 vcc, 1.0, v216
	s_waitcnt vmcnt(4)
	ds_write_b128 v203, v[130:133]
	ds_write_b128 v204, v[134:137]
	ds_write_b128 v201, v[138:141] offset:32768
	ds_write_b128 v202, v[142:145] offset:32768
	s_cbranch_vccz .LBB0_1184
	s_and_saveexec_b64 s[18:19], s[0:1]
	ds_write_b32 v197, v216 offset:128
	s_or_b64 exec, exec, s[18:19]
	s_waitcnt lgkmcnt(0)
	v_add_u32_e32 v1, v196, v182
	ds_read_b128 v[168:171], v1 offset:224
	ds_read_b128 v[172:175], v1 offset:192
	ds_read_b128 v[218:221], v1 offset:160
	ds_read_b128 v[222:225], v1 offset:128
	s_waitcnt lgkmcnt(3)
	v_pk_mul_f32 v[30:31], v[30:31], v[168:169]
	s_waitcnt lgkmcnt(2)
	v_pk_mul_f32 v[26:27], v[26:27], v[172:173]
	s_waitcnt lgkmcnt(1)
	v_pk_mul_f32 v[22:23], v[22:23], v[218:219]
	v_pk_mul_f32 v[32:33], v[32:33], v[170:171]
	v_pk_mul_f32 v[28:29], v[28:29], v[174:175]
	v_pk_mul_f32 v[24:25], v[24:25], v[220:221]
	s_waitcnt lgkmcnt(0)
	v_pk_mul_f32 v[20:21], v[20:21], v[224:225]
	v_pk_mul_f32 v[18:19], v[18:19], v[222:223]
	v_pk_mul_f32 v[62:63], v[62:63], v[168:169]
	v_pk_mul_f32 v[58:59], v[58:59], v[172:173]
	v_pk_mul_f32 v[54:55], v[54:55], v[218:219]
	v_pk_mul_f32 v[64:65], v[64:65], v[170:171]
	v_pk_mul_f32 v[60:61], v[60:61], v[174:175]
	v_pk_mul_f32 v[56:57], v[56:57], v[220:221]
	v_pk_mul_f32 v[52:53], v[52:53], v[224:225]
	v_pk_mul_f32 v[50:51], v[50:51], v[222:223]
	v_pk_mul_f32 v[46:47], v[46:47], v[168:169]
	v_pk_mul_f32 v[42:43], v[42:43], v[172:173]
	v_pk_mul_f32 v[38:39], v[38:39], v[218:219]
	v_pk_mul_f32 v[48:49], v[48:49], v[170:171]
	v_pk_mul_f32 v[44:45], v[44:45], v[174:175]
	v_pk_mul_f32 v[40:41], v[40:41], v[220:221]
	v_pk_mul_f32 v[36:37], v[36:37], v[224:225]
	v_pk_mul_f32 v[34:35], v[34:35], v[222:223]
	v_pk_mul_f32 v[14:15], v[14:15], v[168:169]
	v_pk_mul_f32 v[10:11], v[10:11], v[172:173]
	v_pk_mul_f32 v[6:7], v[6:7], v[218:219]
	v_pk_mul_f32 v[16:17], v[16:17], v[170:171]
	v_pk_mul_f32 v[12:13], v[12:13], v[174:175]
	v_pk_mul_f32 v[8:9], v[8:9], v[220:221]
	v_pk_mul_f32 v[4:5], v[4:5], v[224:225]
	v_pk_mul_f32 v[2:3], v[2:3], v[222:223]

.LBB0_1186:
	ds_read_b64_tr_b16 v[220:221], v198 offset:0
	ds_read_b64_tr_b16 v[222:223], v198 offset:0x800
	ds_read_b64_tr_b16 v[224:225], v198 offset:0x1000
	ds_read_b64_tr_b16 v[226:227], v198 offset:0x1800
	ds_read_b64_tr_b16 v[228:229], v198 offset:0x2000
	ds_read_b64_tr_b16 v[230:231], v198 offset:0x2800
	ds_read_b64_tr_b16 v[232:233], v198 offset:0x3000
	ds_read_b64_tr_b16 v[234:235], v198 offset:0x3800
	s_waitcnt lgkmcnt(0)
	s_nop 0
	v_mfma_f32_32x32x16_bf16 v[18:33], v[162:165], v[220:223], v[18:33]
	ds_read_b64_tr_b16 v[220:221], v198 offset:0x200
	ds_read_b64_tr_b16 v[222:223], v198 offset:0xa00
	v_mfma_f32_32x32x16_bf16 v[18:33], v[166:169], v[224:227], v[18:33]
	ds_read_b64_tr_b16 v[224:225], v198 offset:0x1200
	ds_read_b64_tr_b16 v[226:227], v198 offset:0x1a00
	v_mfma_f32_32x32x16_bf16 v[18:33], v[170:173], v[228:231], v[18:33]
	ds_read_b64_tr_b16 v[228:229], v198 offset:0x2200
	ds_read_b64_tr_b16 v[230:231], v198 offset:0x2a00
	ds_read_b64_tr_b16 v[236:237], v198 offset:0x3200
	ds_read_b64_tr_b16 v[238:239], v198 offset:0x3a00
	v_mfma_f32_32x32x16_bf16 v[18:33], v[174:177], v[232:235], v[18:33]
	s_waitcnt lgkmcnt(0)
	v_mfma_f32_32x32x16_bf16 v[50:65], v[162:165], v[220:223], v[50:65]
	ds_read_b64_tr_b16 v[220:221], v198 offset:0x400
	ds_read_b64_tr_b16 v[222:223], v198 offset:0xc00
	v_mfma_f32_32x32x16_bf16 v[50:65], v[166:169], v[224:227], v[50:65]
	ds_read_b64_tr_b16 v[224:225], v198 offset:0x1400
	ds_read_b64_tr_b16 v[226:227], v198 offset:0x1c00
	v_mfma_f32_32x32x16_bf16 v[50:65], v[170:173], v[228:231], v[50:65]
	ds_read_b64_tr_b16 v[228:229], v198 offset:0x2400
	ds_read_b64_tr_b16 v[230:231], v198 offset:0x2c00
	ds_read_b64_tr_b16 v[232:233], v198 offset:0x3400
	ds_read_b64_tr_b16 v[234:235], v198 offset:0x3c00
	v_mfma_f32_32x32x16_bf16 v[50:65], v[174:177], v[236:239], v[50:65]
	s_waitcnt lgkmcnt(0)
	v_mfma_f32_32x32x16_bf16 v[34:49], v[162:165], v[220:223], v[34:49]
	ds_read_b64_tr_b16 v[220:221], v198 offset:0x600
	ds_read_b64_tr_b16 v[222:223], v198 offset:0xe00
	v_mfma_f32_32x32x16_bf16 v[34:49], v[166:169], v[224:227], v[34:49]
	ds_read_b64_tr_b16 v[224:225], v198 offset:0x1600
	ds_read_b64_tr_b16 v[226:227], v198 offset:0x1e00
	v_mfma_f32_32x32x16_bf16 v[34:49], v[170:173], v[228:231], v[34:49]
	ds_read_b64_tr_b16 v[228:229], v198 offset:0x2600
	ds_read_b64_tr_b16 v[230:231], v198 offset:0x2e00
	ds_read_b64_tr_b16 v[236:237], v198 offset:0x3600
	ds_read_b64_tr_b16 v[238:239], v198 offset:0x3e00
	v_mfma_f32_32x32x16_bf16 v[34:49], v[174:177], v[232:235], v[34:49]
	s_waitcnt lgkmcnt(0)
	v_mfma_f32_32x32x16_bf16 v[2:17], v[162:165], v[220:223], v[2:17]
	v_max_f32_e32 v1, v83, v83
	v_max_f32_e32 v200, v82, v82
	v_max_f32_e32 v1, v200, v1
	v_max3_f32 v1, v1, v84, v85
	v_max3_f32 v1, v1, v86, v87
	v_max3_f32 v1, v1, v88, v89
	v_max3_f32 v1, v1, v90, v91
	v_max3_f32 v1, v1, v92, v93
	v_mfma_f32_32x32x16_bf16 v[2:17], v[166:169], v[224:227], v[2:17]
	v_max3_f32 v1, v1, v94, v95
	v_max3_f32 v1, v1, v96, v97
	v_max3_f32 v1, v1, v66, v67
	v_max3_f32 v1, v1, v68, v69
	v_max3_f32 v1, v1, v70, v71
	v_max3_f32 v1, v1, v72, v73
	v_max3_f32 v1, v1, v74, v75
	v_max3_f32 v1, v1, v76, v77
	v_mfma_f32_32x32x16_bf16 v[2:17], v[170:173], v[228:231], v[2:17]
	v_max3_f32 v1, v1, v78, v79
	v_max3_f32 v1, v1, v80, v81
	v_mov_b32_e32 v162, v1
	s_nop 1
	v_permlane32_swap_b32_e32 v1, v162
	v_max_f32_e32 v162, v162, v162
	v_max_f32_e32 v1, v1, v1
	v_max_f32_e32 v1, v1, v162
	v_max_f32_e32 v163, v217, v217
	v_max_f32_e32 v163, v163, v1
	v_sub_f32_e32 v162, v1, v217
	v_mfma_f32_32x32x16_bf16 v[2:17], v[174:177], v[236:239], v[2:17]
	v_sub_f32_e32 v1, v217, v163
	v_mul_f32_e32 v1, 0x3e0293ee, v1
	v_exp_f32_e32 v1, v1
	v_cmp_ge_f32_e32 vcc, s22, v162
	s_cmp_eq_u64 vcc, exec
	s_cselect_b64 s[2:3], -1, 0
	s_barrier
	s_waitcnt vmcnt(4)
	v_cndmask_b32_e64 v162, v1, 1.0, s[2:3]
	v_cmp_gt_f32_e32 vcc, 1.0, v162
	ds_write_b128 v203, v[146:149] offset:16384
	ds_write_b128 v204, v[150:153] offset:16384
	ds_write_b128 v201, v[154:157] offset:49152
	ds_write_b128 v202, v[158:161] offset:49152
	s_cbranch_vccz .LBB0_1190
	s_and_saveexec_b64 s[20:21], s[0:1]
	ds_write_b32 v197, v162 offset:128
	s_or_b64 exec, exec, s[20:21]
	s_waitcnt lgkmcnt(0)
	v_add_u32_e32 v1, v196, v182
	ds_read_b128 v[146:149], v1 offset:224
	ds_read_b128 v[150:153], v1 offset:192
	ds_read_b128 v[154:157], v1 offset:160
	ds_read_b128 v[158:161], v1 offset:128
	s_waitcnt lgkmcnt(3)
	v_pk_mul_f32 v[30:31], v[30:31], v[146:147]
	s_waitcnt lgkmcnt(2)
	v_pk_mul_f32 v[26:27], v[26:27], v[150:151]
	s_waitcnt lgkmcnt(1)
	v_pk_mul_f32 v[22:23], v[22:23], v[154:155]
	v_pk_mul_f32 v[32:33], v[32:33], v[148:149]
	v_pk_mul_f32 v[28:29], v[28:29], v[152:153]
	v_pk_mul_f32 v[24:25], v[24:25], v[156:157]
	s_waitcnt lgkmcnt(0)
	v_pk_mul_f32 v[20:21], v[20:21], v[160:161]
	v_pk_mul_f32 v[18:19], v[18:19], v[158:159]
	v_pk_mul_f32 v[62:63], v[62:63], v[146:147]
	v_pk_mul_f32 v[58:59], v[58:59], v[150:151]
	v_pk_mul_f32 v[54:55], v[54:55], v[154:155]
	v_pk_mul_f32 v[64:65], v[64:65], v[148:149]
	v_pk_mul_f32 v[60:61], v[60:61], v[152:153]
	v_pk_mul_f32 v[56:57], v[56:57], v[156:157]
	v_pk_mul_f32 v[52:53], v[52:53], v[160:161]
	v_pk_mul_f32 v[50:51], v[50:51], v[158:159]
	v_pk_mul_f32 v[46:47], v[46:47], v[146:147]
	v_pk_mul_f32 v[42:43], v[42:43], v[150:151]
	v_pk_mul_f32 v[38:39], v[38:39], v[154:155]
	v_pk_mul_f32 v[48:49], v[48:49], v[148:149]
	v_pk_mul_f32 v[44:45], v[44:45], v[152:153]
	v_pk_mul_f32 v[40:41], v[40:41], v[156:157]
	v_pk_mul_f32 v[36:37], v[36:37], v[160:161]
	v_pk_mul_f32 v[34:35], v[34:35], v[158:159]
	v_pk_mul_f32 v[14:15], v[14:15], v[146:147]
	v_pk_mul_f32 v[10:11], v[10:11], v[150:151]
	v_pk_mul_f32 v[6:7], v[6:7], v[154:155]
	v_pk_mul_f32 v[16:17], v[16:17], v[148:149]
	v_pk_mul_f32 v[12:13], v[12:13], v[152:153]
	v_pk_mul_f32 v[8:9], v[8:9], v[156:157]
	v_pk_mul_f32 v[4:5], v[4:5], v[160:161]
	v_pk_mul_f32 v[2:3], v[2:3], v[158:159]

.LBB0_1196:
	v_exp_f32_e32 v100, v82
	v_exp_f32_e32 v101, v83
	v_exp_f32_e32 v82, v84
	v_fmamk_f32 v66, v66, 0x3e0293ee, v99
	v_exp_f32_e32 v84, v85
	v_fmamk_f32 v113, v77, 0x3e0293ee, v99
	v_exp_f32_e32 v77, v86
	v_exp_f32_e32 v1, v66
	v_add_f32_e32 v66, 0, v100
	v_exp_f32_e32 v83, v87
	v_add_f32_e32 v66, v101, v66
	v_fmamk_f32 v112, v76, 0x3e0293ee, v99
	v_exp_f32_e32 v76, v88
	v_add_f32_e32 v66, v82, v66
	v_fmamk_f32 v114, v78, 0x3e0293ee, v99
	v_exp_f32_e32 v78, v89
	v_add_f32_e32 v66, v84, v66
	v_fmamk_f32 v107, v73, 0x3e0293ee, v99
	v_exp_f32_e32 v73, v90
	v_add_f32_e32 v66, v77, v66
	v_fmamk_f32 v109, v75, 0x3e0293ee, v99
	v_exp_f32_e32 v75, v91
	v_add_f32_e32 v66, v83, v66
	v_fmamk_f32 v105, v71, 0x3e0293ee, v99
	v_exp_f32_e32 v71, v92
	v_add_f32_e32 v66, v76, v66
	v_fmamk_f32 v108, v74, 0x3e0293ee, v99
	v_exp_f32_e32 v74, v93
	v_add_f32_e32 v66, v78, v66
	v_fmamk_f32 v103, v69, 0x3e0293ee, v99
	v_exp_f32_e32 v69, v94
	v_add_f32_e32 v66, v73, v66
	v_fmamk_f32 v106, v72, 0x3e0293ee, v99
	v_exp_f32_e32 v72, v95
	v_add_f32_e32 v66, v75, v66
	v_fmamk_f32 v102, v68, 0x3e0293ee, v99
	v_exp_f32_e32 v68, v96
	v_add_f32_e32 v66, v71, v66
	v_fmamk_f32 v104, v70, 0x3e0293ee, v99
	v_exp_f32_e32 v70, v97
	v_add_f32_e32 v66, v74, v66
	v_fmamk_f32 v67, v67, 0x3e0293ee, v99
	v_add_f32_e32 v66, v69, v66
	v_exp_f32_e32 v85, v67
	v_add_f32_e32 v66, v72, v66
	v_exp_f32_e32 v86, v102
	v_add_f32_e32 v66, v68, v66
	v_exp_f32_e32 v87, v103
	v_add_f32_e32 v66, v70, v66
	v_exp_f32_e32 v88, v104
	v_add_f32_e32 v66, v1, v66
	v_exp_f32_e32 v89, v105
	v_add_f32_e32 v66, v85, v66
	v_exp_f32_e32 v90, v106
	v_add_f32_e32 v66, v86, v66
	v_exp_f32_e32 v91, v107
	v_add_f32_e32 v66, v87, v66
	v_exp_f32_e32 v92, v108
	v_add_f32_e32 v66, v88, v66
	v_exp_f32_e32 v93, v109
	v_add_f32_e32 v66, v89, v66
	v_exp_f32_e32 v94, v112
	v_add_f32_e32 v66, v90, v66
	v_exp_f32_e32 v95, v113
	v_add_f32_e32 v66, v91, v66
	v_fmamk_f32 v79, v79, 0x3e0293ee, v99
	v_exp_f32_e32 v96, v114
	v_add_f32_e32 v66, v92, v66
	v_fmamk_f32 v80, v80, 0x3e0293ee, v99
	v_exp_f32_e32 v97, v79
	v_add_f32_e32 v66, v93, v66
	v_fmac_f32_e32 v99, 0x3e0293ee, v81
	v_exp_f32_e32 v102, v80
	v_add_f32_e32 v66, v94, v66
	v_exp_f32_e32 v99, v99
	v_add_f32_e32 v66, v95, v66
	v_add_f32_e32 v66, v96, v66
	v_add_f32_e32 v66, v97, v66
	v_add_f32_e32 v66, v102, v66
	v_add_f32_e32 v66, v99, v66
	v_mov_b32_e32 v67, v66
	s_nop 1
	v_permlane32_swap_b32_e32 v66, v67
	v_cvt_pk_bf16_f32 v80, v100, v101
	v_cvt_pk_bf16_f32 v81, v82, v84
	v_cvt_pk_bf16_f32 v82, v77, v83
	v_cvt_pk_bf16_f32 v83, v76, v78
	v_cvt_pk_bf16_f32 v76, v73, v75
	v_cvt_pk_bf16_f32 v77, v71, v74
	v_cvt_pk_bf16_f32 v78, v69, v72
	v_cvt_pk_bf16_f32 v79, v68, v70
	v_cvt_pk_bf16_f32 v68, v1, v85
	v_cvt_pk_bf16_f32 v69, v86, v87
	v_cvt_pk_bf16_f32 v70, v88, v89
	v_cvt_pk_bf16_f32 v71, v90, v91
	v_cvt_pk_bf16_f32 v72, v92, v93
	v_cvt_pk_bf16_f32 v73, v94, v95
	v_cvt_pk_bf16_f32 v74, v96, v97
	v_cvt_pk_bf16_f32 v75, v102, v99
	s_nop 0
	v_permlane32_swap_b32_e32 v80, v82
	v_permlane32_swap_b32_e32 v81, v83
	v_permlane32_swap_b32_e32 v76, v78
	v_permlane32_swap_b32_e32 v77, v79
	v_permlane32_swap_b32_e32 v68, v70
	v_permlane32_swap_b32_e32 v69, v71
	v_permlane32_swap_b32_e32 v72, v74
	v_permlane32_swap_b32_e32 v73, v75
	ds_read_b64_tr_b16 v[84:85], v198 offset:0
	ds_read_b64_tr_b16 v[86:87], v198 offset:0x800
	ds_read_b64_tr_b16 v[88:89], v198 offset:0x1000
	ds_read_b64_tr_b16 v[90:91], v198 offset:0x1800
	ds_read_b64_tr_b16 v[92:93], v198 offset:0x2000
	ds_read_b64_tr_b16 v[94:95], v198 offset:0x2800
	ds_read_b64_tr_b16 v[100:101], v198 offset:0x3000
	ds_read_b64_tr_b16 v[102:103], v198 offset:0x3800
	s_waitcnt lgkmcnt(0)
	s_nop 0
	v_mfma_f32_32x32x16_bf16 v[18:33], v[80:83], v[84:87], v[18:33]
	ds_read_b64_tr_b16 v[84:85], v198 offset:0x200
	ds_read_b64_tr_b16 v[86:87], v198 offset:0xa00
	v_mfma_f32_32x32x16_bf16 v[18:33], v[76:79], v[88:91], v[18:33]
	ds_read_b64_tr_b16 v[88:89], v198 offset:0x1200
	ds_read_b64_tr_b16 v[90:91], v198 offset:0x1a00
	v_mfma_f32_32x32x16_bf16 v[18:33], v[68:71], v[92:95], v[18:33]
	ds_read_b64_tr_b16 v[92:93], v198 offset:0x2200
	ds_read_b64_tr_b16 v[94:95], v198 offset:0x2a00
	ds_read_b64_tr_b16 v[104:105], v198 offset:0x3200
	ds_read_b64_tr_b16 v[106:107], v198 offset:0x3a00
	v_mfma_f32_32x32x16_bf16 v[18:33], v[72:75], v[100:103], v[18:33]
	s_waitcnt lgkmcnt(0)
	v_mfma_f32_32x32x16_bf16 v[50:65], v[80:83], v[84:87], v[50:65]
	ds_read_b64_tr_b16 v[84:85], v198 offset:0x400
	ds_read_b64_tr_b16 v[86:87], v198 offset:0xc00
	v_mfma_f32_32x32x16_bf16 v[50:65], v[76:79], v[88:91], v[50:65]
	ds_read_b64_tr_b16 v[88:89], v198 offset:0x1400
	ds_read_b64_tr_b16 v[90:91], v198 offset:0x1c00
	v_mfma_f32_32x32x16_bf16 v[50:65], v[68:71], v[92:95], v[50:65]
	ds_read_b64_tr_b16 v[92:93], v198 offset:0x2400
	ds_read_b64_tr_b16 v[94:95], v198 offset:0x2c00
	ds_read_b64_tr_b16 v[100:101], v198 offset:0x3400
	ds_read_b64_tr_b16 v[102:103], v198 offset:0x3c00
	v_mfma_f32_32x32x16_bf16 v[50:65], v[72:75], v[104:107], v[50:65]
	s_waitcnt lgkmcnt(0)
	v_mfma_f32_32x32x16_bf16 v[34:49], v[80:83], v[84:87], v[34:49]
	ds_read_b64_tr_b16 v[84:85], v198 offset:0x600
	ds_read_b64_tr_b16 v[86:87], v198 offset:0xe00
	v_mfma_f32_32x32x16_bf16 v[34:49], v[76:79], v[88:91], v[34:49]
	ds_read_b64_tr_b16 v[88:89], v198 offset:0x1600
	ds_read_b64_tr_b16 v[90:91], v198 offset:0x1e00
	v_mfma_f32_32x32x16_bf16 v[34:49], v[68:71], v[92:95], v[34:49]
	ds_read_b64_tr_b16 v[92:93], v198 offset:0x2600
	ds_read_b64_tr_b16 v[94:95], v198 offset:0x2e00
	ds_read_b64_tr_b16 v[104:105], v198 offset:0x3600
	ds_read_b64_tr_b16 v[106:107], v198 offset:0x3e00
	v_mfma_f32_32x32x16_bf16 v[34:49], v[72:75], v[100:103], v[34:49]
	s_waitcnt lgkmcnt(0)
	v_mfma_f32_32x32x16_bf16 v[2:17], v[80:83], v[84:87], v[2:17]
	v_mfma_f32_32x32x16_bf16 v[2:17], v[76:79], v[88:91], v[2:17]
	v_mfma_f32_32x32x16_bf16 v[2:17], v[68:71], v[92:95], v[2:17]
	v_mfma_f32_32x32x16_bf16 v[2:17], v[72:75], v[104:107], v[2:17]
	s_and_saveexec_b64 s[2:3], s[0:1]
	v_add_f32_e32 v1, v110, v111
	v_fmac_f32_e32 v1, v183, v162
	v_add_f32_e32 v66, v66, v67
	v_fmac_f32_e32 v66, v1, v98
	ds_write_b32 v197, v66
	s_or_b64 exec, exec, s[2:3]
	s_waitcnt lgkmcnt(0)
	v_add_u32_e32 v1, v196, v182
	ds_read_b128 v[66:69], v1
	ds_read_b128 v[70:73], v1 offset:32
	s_add_u32 s0, s4, s10
	s_addc_u32 s1, s5, s11
	s_add_i32 s2, 0, 0x10800
	s_waitcnt lgkmcnt(1)
	v_rcp_f32_e32 v74, v66
	v_rcp_f32_e32 v75, v67
	v_rcp_f32_e32 v76, v68
	v_rcp_f32_e32 v77, v69
	s_waitcnt lgkmcnt(0)
	v_rcp_f32_e32 v78, v70
	ds_read_b128 v[66:69], v1 offset:64
	v_rcp_f32_e32 v79, v71
	v_rcp_f32_e32 v80, v72
	v_rcp_f32_e32 v81, v73
	ds_read_b128 v[70:73], v1 offset:96
	s_waitcnt lgkmcnt(1)
	v_rcp_f32_e32 v1, v66
	v_rcp_f32_e32 v66, v67
	v_rcp_f32_e32 v67, v68
	v_rcp_f32_e32 v68, v69
	s_waitcnt lgkmcnt(0)
	v_rcp_f32_e32 v69, v70
	v_rcp_f32_e32 v70, v71
	v_rcp_f32_e32 v71, v72
	v_rcp_f32_e32 v72, v73
	v_lshl_add_u32 v73, v181, 13, s2
	v_mul_f32_e32 v18, v18, v74
	s_mov_b32 s2, 0xc3e00000
	v_mov_b32_e32 v83, 0x43e00000
	v_mul_f32_e32 v19, v19, v75
	v_med3_f32 v18, v18, s2, v83
	v_med3_f32 v19, v19, s2, v83
	v_mov_b32_e32 v84, 0
	v_cvt_pk_fp8_f32 v84, v18, v19
	v_mul_f32_e32 v18, v20, v76
	v_mul_f32_e32 v19, v21, v77
	v_med3_f32 v18, v18, s2, v83
	v_med3_f32 v19, v19, s2, v83
	v_mov_b32_e32 v20, 0
	v_cvt_pk_fp8_f32 v20, v18, v19
	v_lshlrev_b32_e32 v82, 9, v193
	v_add3_u32 v82, v73, v82, v179
	v_lshrrev_b32_e32 v18, 8, v84
	ds_write_b8 v82, v84
	ds_write_b8 v82, v18 offset:128
	ds_write_b8 v82, v20 offset:256
	v_lshrrev_b32_e32 v18, 8, v20
	ds_write_b8 v82, v18 offset:384
	v_mul_f32_e32 v18, v22, v78
	v_mul_f32_e32 v19, v23, v79
	v_med3_f32 v18, v18, s2, v83
	v_med3_f32 v19, v19, s2, v83
	v_mov_b32_e32 v20, 0
	v_cvt_pk_fp8_f32 v20, v18, v19
	v_mul_f32_e32 v18, v24, v80
	v_mul_f32_e32 v19, v25, v81
	v_med3_f32 v18, v18, s2, v83
	v_med3_f32 v19, v19, s2, v83
	v_mov_b32_e32 v21, 0
	v_cvt_pk_fp8_f32 v21, v18, v19
	v_lshrrev_b32_e32 v18, 8, v20
	ds_write_b8 v82, v20 offset:1024
	ds_write_b8 v82, v18 offset:1152
	ds_write_b8 v82, v21 offset:1280
	v_lshrrev_b32_e32 v18, 8, v21
	ds_write_b8 v82, v18 offset:1408
	v_mul_f32_e32 v18, v26, v1
	v_mul_f32_e32 v19, v27, v66
	v_med3_f32 v18, v18, s2, v83
	v_med3_f32 v19, v19, s2, v83
	v_mov_b32_e32 v20, 0
	v_cvt_pk_fp8_f32 v20, v18, v19
	v_mul_f32_e32 v18, v28, v67
	v_mul_f32_e32 v19, v29, v68
	v_med3_f32 v18, v18, s2, v83
	v_med3_f32 v19, v19, s2, v83
	v_mov_b32_e32 v21, 0
	v_cvt_pk_fp8_f32 v21, v18, v19
	v_lshrrev_b32_e32 v18, 8, v20
	ds_write_b8 v82, v20 offset:2048
	ds_write_b8 v82, v18 offset:2176
	ds_write_b8 v82, v21 offset:2304
	v_lshrrev_b32_e32 v18, 8, v21
	ds_write_b8 v82, v18 offset:2432
	v_mul_f32_e32 v18, v30, v69
	v_mul_f32_e32 v19, v31, v70
	v_med3_f32 v18, v18, s2, v83
	v_med3_f32 v19, v19, s2, v83
	v_mov_b32_e32 v20, 0
	v_cvt_pk_fp8_f32 v20, v18, v19
	v_mul_f32_e32 v18, v32, v71
	v_mul_f32_e32 v19, v33, v72
	v_med3_f32 v18, v18, s2, v83
	v_med3_f32 v19, v19, s2, v83
	v_mov_b32_e32 v21, 0
	v_cvt_pk_fp8_f32 v21, v18, v19
	v_lshrrev_b32_e32 v18, 8, v20
	ds_write_b8 v82, v20 offset:3072
	ds_write_b8 v82, v18 offset:3200
	ds_write_b8 v82, v21 offset:3328
	v_lshrrev_b32_e32 v18, 8, v21
	ds_write_b8 v82, v18 offset:3456
	v_mul_f32_e32 v18, v50, v74
	v_mul_f32_e32 v19, v51, v75
	v_med3_f32 v18, v18, s2, v83
	v_med3_f32 v19, v19, s2, v83
	v_mov_b32_e32 v20, 0
	v_cvt_pk_fp8_f32 v20, v18, v19
	v_mul_f32_e32 v18, v52, v76
	v_mul_f32_e32 v19, v53, v77
	v_med3_f32 v18, v18, s2, v83
	v_med3_f32 v19, v19, s2, v83
	v_mov_b32_e32 v21, 0
	v_cvt_pk_fp8_f32 v21, v18, v19
	v_lshrrev_b32_e32 v18, 8, v20
	ds_write_b8 v82, v20 offset:32
	ds_write_b8 v82, v18 offset:160
	ds_write_b8 v82, v21 offset:288
	v_lshrrev_b32_e32 v18, 8, v21
	ds_write_b8 v82, v18 offset:416
	v_mul_f32_e32 v18, v54, v78
	v_mul_f32_e32 v19, v55, v79
	v_med3_f32 v18, v18, s2, v83
	v_med3_f32 v19, v19, s2, v83
	v_mov_b32_e32 v20, 0
	v_cvt_pk_fp8_f32 v20, v18, v19
	v_mul_f32_e32 v18, v56, v80
	v_mul_f32_e32 v19, v57, v81
	v_med3_f32 v18, v18, s2, v83
	v_med3_f32 v19, v19, s2, v83
	v_mov_b32_e32 v21, 0
	v_cvt_pk_fp8_f32 v21, v18, v19
	v_lshrrev_b32_e32 v18, 8, v20
	ds_write_b8 v82, v20 offset:1056
	ds_write_b8 v82, v18 offset:1184
	ds_write_b8 v82, v21 offset:1312
	v_lshrrev_b32_e32 v18, 8, v21
	ds_write_b8 v82, v18 offset:1440
	v_mul_f32_e32 v18, v58, v1
	v_mul_f32_e32 v19, v59, v66
	v_med3_f32 v18, v18, s2, v83
	v_med3_f32 v19, v19, s2, v83
	v_mov_b32_e32 v20, 0
	v_cvt_pk_fp8_f32 v20, v18, v19
	v_mul_f32_e32 v18, v60, v67
	v_mul_f32_e32 v19, v61, v68
	v_med3_f32 v18, v18, s2, v83
	v_med3_f32 v19, v19, s2, v83
	v_mov_b32_e32 v21, 0
	v_cvt_pk_fp8_f32 v21, v18, v19
	v_lshrrev_b32_e32 v18, 8, v20
	ds_write_b8 v82, v20 offset:2080
	ds_write_b8 v82, v18 offset:2208
	ds_write_b8 v82, v21 offset:2336
	v_lshrrev_b32_e32 v18, 8, v21
	ds_write_b8 v82, v18 offset:2464
	v_mul_f32_e32 v18, v62, v69
	v_mul_f32_e32 v19, v63, v70
	v_med3_f32 v18, v18, s2, v83
	v_med3_f32 v19, v19, s2, v83
	v_mov_b32_e32 v20, 0
	v_cvt_pk_fp8_f32 v20, v18, v19
	v_mul_f32_e32 v18, v64, v71
	v_mul_f32_e32 v19, v65, v72
	v_med3_f32 v18, v18, s2, v83
	v_med3_f32 v19, v19, s2, v83
	v_mov_b32_e32 v21, 0
	v_cvt_pk_fp8_f32 v21, v18, v19
	v_lshrrev_b32_e32 v18, 8, v20
	ds_write_b8 v82, v20 offset:3104
	ds_write_b8 v82, v18 offset:3232
	ds_write_b8 v82, v21 offset:3360
	v_lshrrev_b32_e32 v18, 8, v21
	ds_write_b8 v82, v18 offset:3488
	v_mul_f32_e32 v18, v34, v74
	v_mul_f32_e32 v19, v35, v75
	v_med3_f32 v18, v18, s2, v83
	v_med3_f32 v19, v19, s2, v83
	v_mov_b32_e32 v20, 0
	v_cvt_pk_fp8_f32 v20, v18, v19
	v_mul_f32_e32 v18, v36, v76
	v_mul_f32_e32 v19, v37, v77
	v_med3_f32 v18, v18, s2, v83
	v_med3_f32 v19, v19, s2, v83
	v_mov_b32_e32 v21, 0
	v_cvt_pk_fp8_f32 v21, v18, v19
	v_lshrrev_b32_e32 v18, 8, v20
	ds_write_b8 v82, v20 offset:64
	ds_write_b8 v82, v18 offset:192
	ds_write_b8 v82, v21 offset:320
	v_lshrrev_b32_e32 v18, 8, v21
	ds_write_b8 v82, v18 offset:448
	v_mul_f32_e32 v18, v38, v78
	v_mul_f32_e32 v19, v39, v79
	v_med3_f32 v18, v18, s2, v83
	v_med3_f32 v19, v19, s2, v83
	v_mov_b32_e32 v20, 0
	v_cvt_pk_fp8_f32 v20, v18, v19
	v_mul_f32_e32 v18, v40, v80
	v_mul_f32_e32 v19, v41, v81
	v_med3_f32 v18, v18, s2, v83
	v_med3_f32 v19, v19, s2, v83
	v_mov_b32_e32 v21, 0
	v_cvt_pk_fp8_f32 v21, v18, v19
	v_lshrrev_b32_e32 v18, 8, v20
	ds_write_b8 v82, v20 offset:1088
	ds_write_b8 v82, v18 offset:1216
	ds_write_b8 v82, v21 offset:1344
	v_lshrrev_b32_e32 v18, 8, v21
	ds_write_b8 v82, v18 offset:1472
	v_mul_f32_e32 v18, v42, v1
	v_mul_f32_e32 v19, v43, v66
	v_med3_f32 v18, v18, s2, v83
	v_med3_f32 v19, v19, s2, v83
	v_mov_b32_e32 v20, 0
	v_cvt_pk_fp8_f32 v20, v18, v19
	v_mul_f32_e32 v18, v44, v67
	v_mul_f32_e32 v19, v45, v68
	v_med3_f32 v18, v18, s2, v83
	v_med3_f32 v19, v19, s2, v83
	v_mov_b32_e32 v21, 0
	v_cvt_pk_fp8_f32 v21, v18, v19
	v_lshrrev_b32_e32 v18, 8, v20
	ds_write_b8 v82, v20 offset:2112
	ds_write_b8 v82, v18 offset:2240
	ds_write_b8 v82, v21 offset:2368
	v_lshrrev_b32_e32 v18, 8, v21
	ds_write_b8 v82, v18 offset:2496
	v_mul_f32_e32 v18, v46, v69
	v_mul_f32_e32 v19, v47, v70
	v_med3_f32 v18, v18, s2, v83
	v_med3_f32 v19, v19, s2, v83
	v_mov_b32_e32 v20, 0
	v_cvt_pk_fp8_f32 v20, v18, v19
	v_mul_f32_e32 v18, v48, v71
	v_mul_f32_e32 v19, v49, v72
	v_med3_f32 v18, v18, s2, v83
	v_med3_f32 v19, v19, s2, v83
	v_mov_b32_e32 v21, 0
	v_cvt_pk_fp8_f32 v21, v18, v19
	v_lshrrev_b32_e32 v18, 8, v20
	ds_write_b8 v82, v20 offset:3136
	ds_write_b8 v82, v18 offset:3264
	ds_write_b8 v82, v21 offset:3392
	v_lshrrev_b32_e32 v18, 8, v21
	v_mul_f32_e32 v2, v2, v74
	v_mul_f32_e32 v3, v3, v75
	ds_write_b8 v82, v18 offset:3520
	v_med3_f32 v2, v2, s2, v83
	v_med3_f32 v3, v3, s2, v83
	v_mov_b32_e32 v18, 0
	v_cvt_pk_fp8_f32 v18, v2, v3
	v_mul_f32_e32 v2, v4, v76
	v_mul_f32_e32 v3, v5, v77
	v_med3_f32 v2, v2, s2, v83
	v_med3_f32 v3, v3, s2, v83
	v_mov_b32_e32 v4, 0
	v_cvt_pk_fp8_f32 v4, v2, v3
	v_lshrrev_b32_e32 v2, 8, v18
	ds_write_b8 v82, v18 offset:96
	ds_write_b8 v82, v2 offset:224
	ds_write_b8 v82, v4 offset:352
	v_lshrrev_b32_e32 v2, 8, v4
	ds_write_b8 v82, v2 offset:480
	v_mul_f32_e32 v2, v6, v78
	v_mul_f32_e32 v3, v7, v79
	v_med3_f32 v2, v2, s2, v83
	v_med3_f32 v3, v3, s2, v83
	v_mov_b32_e32 v4, 0
	v_cvt_pk_fp8_f32 v4, v2, v3
	v_mul_f32_e32 v2, v8, v80
	v_mul_f32_e32 v3, v9, v81
	v_med3_f32 v2, v2, s2, v83
	v_med3_f32 v3, v3, s2, v83
	v_mov_b32_e32 v5, 0
	v_cvt_pk_fp8_f32 v5, v2, v3
	v_lshrrev_b32_e32 v2, 8, v4
	ds_write_b8 v82, v4 offset:1120
	ds_write_b8 v82, v2 offset:1248
	ds_write_b8 v82, v5 offset:1376
	v_lshrrev_b32_e32 v2, 8, v5
	ds_write_b8 v82, v2 offset:1504
	v_mul_f32_e32 v1, v10, v1
	v_mul_f32_e32 v2, v11, v66
	v_med3_f32 v1, v1, s2, v83
	v_med3_f32 v2, v2, s2, v83
	v_mov_b32_e32 v3, 0
	v_cvt_pk_fp8_f32 v3, v1, v2
	v_mul_f32_e32 v1, v12, v67
	v_mul_f32_e32 v2, v13, v68
	v_med3_f32 v1, v1, s2, v83
	v_med3_f32 v2, v2, s2, v83
	v_mov_b32_e32 v4, 0
	v_cvt_pk_fp8_f32 v4, v1, v2
	v_lshrrev_b32_e32 v1, 8, v3
	ds_write_b8 v82, v3 offset:2144
	ds_write_b8 v82, v1 offset:2272
	ds_write_b8 v82, v4 offset:2400
	v_lshrrev_b32_e32 v1, 8, v4
	ds_write_b8 v82, v1 offset:2528
	v_mul_f32_e32 v1, v14, v69
	v_mul_f32_e32 v2, v15, v70
	v_med3_f32 v1, v1, s2, v83
	v_med3_f32 v2, v2, s2, v83
	v_mov_b32_e32 v3, 0
	v_cvt_pk_fp8_f32 v3, v1, v2
	v_mul_f32_e32 v1, v16, v71
	v_mul_f32_e32 v2, v17, v72
	v_med3_f32 v1, v1, s2, v83
	v_med3_f32 v2, v2, s2, v83
	v_mov_b32_e32 v4, 0
	v_cvt_pk_fp8_f32 v4, v1, v2
	v_lshrrev_b32_e32 v1, 8, v3
	ds_write_b8 v82, v3 offset:3168
	ds_write_b8 v82, v1 offset:3296
	ds_write_b8 v82, v4 offset:3424
	v_lshrrev_b32_e32 v1, 8, v4
	ds_write_b8 v82, v1 offset:3552
	v_lshrrev_b32_e32 v1, 3, v254
	v_lshlrev_b32_e32 v2, 7, v1
	v_mov_b32_e32 v181, 0
	s_waitcnt lgkmcnt(0)
	v_add3_u32 v14, v73, v2, v178
	v_lshl_add_u64 v[6:7], s[0:1], 0, v[180:181]
	v_lshlrev_b32_e32 v180, 11, v1
	ds_read_b128 v[2:5], v14
	v_lshl_add_u64 v[6:7], v[6:7], 0, v[180:181]
	v_mov_b32_e32 v179, v181
	v_lshl_add_u64 v[10:11], v[6:7], 0, v[178:179]
	ds_read_b128 v[6:9], v14 offset:1024
	s_movk_i32 s0, 0x4000
	s_waitcnt lgkmcnt(1)
	global_store_dwordx4 v[10:11], v[2:5], off
	s_nop 1
	v_add_co_u32_e32 v2, vcc, s0, v10
	s_nop 1
	v_addc_co_u32_e32 v3, vcc, 0, v11, vcc
	s_waitcnt lgkmcnt(0)
	global_store_dwordx4 v[2:3], v[6:9], off
	ds_read_b128 v[2:5], v14 offset:2048
	ds_read_b128 v[6:9], v14 offset:3072
	v_add_co_u32_e32 v12, vcc, 0x8000, v10
	s_nop 1
	v_addc_co_u32_e32 v13, vcc, 0, v11, vcc
	s_waitcnt lgkmcnt(1)
	global_store_dwordx4 v[12:13], v[2:5], off
	s_nop 1
	v_add_co_u32_e32 v2, vcc, 0xc000, v10
	s_nop 1
	v_addc_co_u32_e32 v3, vcc, 0, v11, vcc
	s_waitcnt lgkmcnt(0)
	global_store_dwordx4 v[2:3], v[6:9], off
	s_waitcnt lgkmcnt(0)
	s_barrier
	s_lshl_b32 s0, s33, 1
	s_add_i32 s56, s76, s0
	s_cmpk_gt_i32 s56, 0x1ff
	s_cbranch_scc1 .LBB0_1220

.LBB0_1202:
	ds_read_b128 v[66:69], v206 offset:49152
	ds_read_b128 v[70:73], v206 offset:57344
	ds_read_b128 v[230:233], v207 offset:49152
	ds_read_b128 v[234:237], v207 offset:57344
	v_exp_f32_e32 v1, v156
	v_exp_f32_e32 v156, v157
	s_waitcnt lgkmcnt(3)
	v_mfma_f32_32x32x16_bf16 v[82:97], v[66:69], v[126:129], 0
	v_exp_f32_e32 v157, v160
	v_exp_f32_e32 v160, v161
	v_add_f32_e32 v161, 0, v177
	v_add_f32_e32 v161, v228, v161
	v_add_f32_e32 v161, v163, v161
	v_add_f32_e32 v161, v225, v161
	v_add_f32_e32 v161, v164, v161
	s_waitcnt lgkmcnt(2)
	v_mfma_f32_32x32x16_bf16 v[66:81], v[70:73], v[126:129], 0
	v_add_f32_e32 v161, v176, v161
	v_add_f32_e32 v161, v165, v161
	v_add_f32_e32 v161, v175, v161
	v_add_f32_e32 v161, v172, v161
	v_add_f32_e32 v161, v174, v161
	v_add_f32_e32 v161, v171, v161
	v_add_f32_e32 v161, v173, v161
	s_waitcnt lgkmcnt(1)
	v_mfma_f32_32x32x16_bf16 v[82:97], v[230:233], v[122:125], v[82:97]
	v_add_f32_e32 v161, v168, v161
	v_add_f32_e32 v161, v170, v161
	v_exp_f32_e32 v154, v154
	v_add_f32_e32 v161, v167, v161
	v_exp_f32_e32 v155, v155
	v_add_f32_e32 v161, v169, v161
	v_exp_f32_e32 v150, v150
	s_waitcnt lgkmcnt(0)
	v_mfma_f32_32x32x16_bf16 v[66:81], v[234:237], v[122:125], v[66:81]
	ds_read_b128 v[230:233], v208 offset:49152
	ds_read_b128 v[234:237], v208 offset:57344
	v_add_f32_e32 v161, v1, v161
	v_exp_f32_e32 v151, v151
	v_add_f32_e32 v161, v156, v161
	v_exp_f32_e32 v148, v148
	v_add_f32_e32 v161, v154, v161
	v_exp_f32_e32 v149, v149
	s_waitcnt lgkmcnt(1)
	v_mfma_f32_32x32x16_bf16 v[82:97], v[230:233], v[118:121], v[82:97]
	v_add_f32_e32 v161, v155, v161
	v_exp_f32_e32 v146, v146
	v_add_f32_e32 v161, v150, v161
	v_exp_f32_e32 v147, v147
	v_add_f32_e32 v161, v151, v161
	v_add_f32_e32 v161, v148, v161
	v_add_f32_e32 v161, v149, v161
	s_waitcnt lgkmcnt(0)
	v_mfma_f32_32x32x16_bf16 v[66:81], v[234:237], v[118:121], v[66:81]
	ds_read_b128 v[230:233], v209 offset:49152
	ds_read_b128 v[234:237], v209 offset:57344
	v_exp_f32_e32 v158, v158
	v_add_f32_e32 v161, v146, v161
	v_exp_f32_e32 v159, v159
	v_add_f32_e32 v161, v147, v161
	v_exp_f32_e32 v152, v152
	v_add_f32_e32 v161, v157, v161
	s_waitcnt lgkmcnt(1)
	v_mfma_f32_32x32x16_bf16 v[82:97], v[230:233], v[114:117], v[82:97]
	v_exp_f32_e32 v153, v153
	v_add_f32_e32 v161, v160, v161
	v_add_f32_e32 v161, v158, v161
	v_add_f32_e32 v161, v159, v161
	v_add_f32_e32 v161, v152, v161
	v_add_f32_e32 v222, v153, v161
	v_mov_b32_e32 v223, v222
	s_waitcnt lgkmcnt(0)
	v_mfma_f32_32x32x16_bf16 v[66:81], v[234:237], v[114:117], v[66:81]
	ds_read_b128 v[230:233], v210 offset:49152
	ds_read_b128 v[234:237], v210 offset:57344
	v_permlane32_swap_b32_e32 v222, v223
	s_waitcnt lgkmcnt(1)
	v_mfma_f32_32x32x16_bf16 v[82:97], v[230:233], v[110:113], v[82:97]
	s_waitcnt lgkmcnt(0)
	v_mfma_f32_32x32x16_bf16 v[66:81], v[234:237], v[110:113], v[66:81]
	ds_read_b128 v[230:233], v211 offset:49152
	ds_read_b128 v[234:237], v211 offset:57344
	s_waitcnt lgkmcnt(1)
	v_mfma_f32_32x32x16_bf16 v[82:97], v[230:233], v[106:109], v[82:97]
	s_waitcnt lgkmcnt(0)
	v_mfma_f32_32x32x16_bf16 v[66:81], v[234:237], v[106:109], v[66:81]
	ds_read_b128 v[230:233], v212 offset:49152
	ds_read_b128 v[234:237], v212 offset:57344
	s_waitcnt lgkmcnt(1)
	v_mfma_f32_32x32x16_bf16 v[82:97], v[230:233], v[102:105], v[82:97]
	s_waitcnt lgkmcnt(0)
	v_mfma_f32_32x32x16_bf16 v[66:81], v[234:237], v[102:105], v[66:81]
	ds_read_b128 v[230:233], v213 offset:49152
	ds_read_b128 v[234:237], v213 offset:57344
	v_cvt_pk_bf16_f32 v162, v177, v228
	v_cvt_pk_bf16_f32 v163, v163, v225
	v_cvt_pk_bf16_f32 v164, v164, v176
	v_cvt_pk_bf16_f32 v165, v165, v175
	v_cvt_pk_bf16_f32 v172, v172, v174
	v_cvt_pk_bf16_f32 v173, v171, v173
	s_waitcnt lgkmcnt(1)
	v_mfma_f32_32x32x16_bf16 v[82:97], v[230:233], v[98:101], v[82:97]
	v_cvt_pk_bf16_f32 v174, v168, v170
	v_cvt_pk_bf16_f32 v175, v167, v169
	v_cvt_pk_bf16_f32 v168, v1, v156
	v_cvt_pk_bf16_f32 v169, v154, v155
	v_cvt_pk_bf16_f32 v170, v150, v151
	v_cvt_pk_bf16_f32 v171, v148, v149
	v_cvt_pk_bf16_f32 v224, v146, v147
	s_waitcnt lgkmcnt(0)
	v_mfma_f32_32x32x16_bf16 v[66:81], v[234:237], v[98:101], v[66:81]
	v_cvt_pk_bf16_f32 v225, v157, v160
	v_cvt_pk_bf16_f32 v226, v158, v159
	v_permlane32_swap_b32_e32 v162, v164
	v_cvt_pk_bf16_f32 v227, v152, v153
	v_permlane32_swap_b32_e32 v224, v226
	v_permlane32_swap_b32_e32 v163, v165
	v_permlane32_swap_b32_e32 v172, v174
	v_permlane32_swap_b32_e32 v173, v175
	v_permlane32_swap_b32_e32 v168, v170
	v_permlane32_swap_b32_e32 v169, v171
	v_permlane32_swap_b32_e32 v225, v227
	v_lshl_add_u64 v[154:155], s[10:11], 0, v[188:189]
	v_add_co_u32_e32 v146, vcc, s58, v154
	v_lshl_add_u64 v[156:157], s[10:11], 0, v[190:191]
	s_nop 0
	v_addc_co_u32_e32 v147, vcc, 0, v155, vcc
	v_add_co_u32_e32 v150, vcc, s58, v156
	s_nop 1
	v_addc_co_u32_e32 v151, vcc, 0, v157, vcc
	v_add_co_u32_e32 v154, vcc, s59, v154
	global_load_dwordx4 v[146:149], v[146:147], off
	s_nop 0
	global_load_dwordx4 v[150:153], v[150:151], off
	v_addc_co_u32_e32 v155, vcc, 0, v155, vcc
	v_add_co_u32_e32 v158, vcc, s59, v156
	s_nop 1
	v_addc_co_u32_e32 v159, vcc, 0, v157, vcc
	global_load_dwordx4 v[154:157], v[154:155], off
	s_nop 0
	global_load_dwordx4 v[158:161], v[158:159], off
	ds_read_b64_tr_b16 v[228:229], v195 offset:0
	ds_read_b64_tr_b16 v[230:231], v195 offset:0x800
	ds_read_b64_tr_b16 v[232:233], v195 offset:0x1000
	ds_read_b64_tr_b16 v[234:235], v195 offset:0x1800
	ds_read_b64_tr_b16 v[236:237], v195 offset:0x2000
	ds_read_b64_tr_b16 v[238:239], v195 offset:0x2800
	ds_read_b64_tr_b16 v[240:241], v195 offset:0x3000
	ds_read_b64_tr_b16 v[242:243], v195 offset:0x3800
	s_waitcnt lgkmcnt(0)
	s_nop 0
	v_mfma_f32_32x32x16_bf16 v[34:49], v[162:165], v[228:231], v[34:49]
	ds_read_b64_tr_b16 v[228:229], v195 offset:0x200
	ds_read_b64_tr_b16 v[230:231], v195 offset:0xa00
	v_mfma_f32_32x32x16_bf16 v[34:49], v[172:175], v[232:235], v[34:49]
	ds_read_b64_tr_b16 v[232:233], v195 offset:0x1200
	ds_read_b64_tr_b16 v[234:235], v195 offset:0x1a00
	v_mfma_f32_32x32x16_bf16 v[34:49], v[168:171], v[236:239], v[34:49]
	ds_read_b64_tr_b16 v[236:237], v195 offset:0x2200
	ds_read_b64_tr_b16 v[238:239], v195 offset:0x2a00
	ds_read_b64_tr_b16 v[244:245], v195 offset:0x3200
	ds_read_b64_tr_b16 v[246:247], v195 offset:0x3a00
	v_mfma_f32_32x32x16_bf16 v[34:49], v[224:227], v[240:243], v[34:49]
	s_waitcnt lgkmcnt(0)
	v_mfma_f32_32x32x16_bf16 v[50:65], v[162:165], v[228:231], v[50:65]
	ds_read_b64_tr_b16 v[228:229], v195 offset:0x400
	ds_read_b64_tr_b16 v[230:231], v195 offset:0xc00
	v_mfma_f32_32x32x16_bf16 v[50:65], v[172:175], v[232:235], v[50:65]
	ds_read_b64_tr_b16 v[232:233], v195 offset:0x1400
	ds_read_b64_tr_b16 v[234:235], v195 offset:0x1c00
	v_mfma_f32_32x32x16_bf16 v[50:65], v[168:171], v[236:239], v[50:65]
	ds_read_b64_tr_b16 v[236:237], v195 offset:0x2400
	ds_read_b64_tr_b16 v[238:239], v195 offset:0x2c00
	ds_read_b64_tr_b16 v[240:241], v195 offset:0x3400
	ds_read_b64_tr_b16 v[242:243], v195 offset:0x3c00
	v_mfma_f32_32x32x16_bf16 v[50:65], v[224:227], v[244:247], v[50:65]
	s_waitcnt lgkmcnt(0)
	v_mfma_f32_32x32x16_bf16 v[18:33], v[162:165], v[228:231], v[18:33]
	ds_read_b64_tr_b16 v[228:229], v195 offset:0x600
	ds_read_b64_tr_b16 v[230:231], v195 offset:0xe00
	v_mfma_f32_32x32x16_bf16 v[18:33], v[172:175], v[232:235], v[18:33]
	ds_read_b64_tr_b16 v[232:233], v195 offset:0x1600
	ds_read_b64_tr_b16 v[234:235], v195 offset:0x1e00
	v_mfma_f32_32x32x16_bf16 v[18:33], v[168:171], v[236:239], v[18:33]
	ds_read_b64_tr_b16 v[236:237], v195 offset:0x2600
	ds_read_b64_tr_b16 v[238:239], v195 offset:0x2e00
	ds_read_b64_tr_b16 v[244:245], v195 offset:0x3600
	ds_read_b64_tr_b16 v[246:247], v195 offset:0x3e00
	v_mfma_f32_32x32x16_bf16 v[18:33], v[224:227], v[240:243], v[18:33]
	s_waitcnt lgkmcnt(0)
	v_mfma_f32_32x32x16_bf16 v[2:17], v[162:165], v[228:231], v[2:17]
	v_max_f32_e32 v1, v83, v83
	v_max_f32_e32 v167, v82, v82
	v_max_f32_e32 v1, v167, v1
	v_max3_f32 v1, v1, v84, v85
	v_max3_f32 v1, v1, v86, v87
	v_max3_f32 v1, v1, v88, v89
	v_max3_f32 v1, v1, v90, v91
	v_max3_f32 v1, v1, v92, v93
	v_mfma_f32_32x32x16_bf16 v[2:17], v[172:175], v[232:235], v[2:17]
	v_max3_f32 v1, v1, v94, v95
	v_max3_f32 v1, v1, v96, v97
	v_max3_f32 v1, v1, v66, v67
	v_max3_f32 v1, v1, v68, v69
	v_max3_f32 v1, v1, v70, v71
	v_max3_f32 v1, v1, v72, v73
	v_max3_f32 v1, v1, v74, v75
	v_max3_f32 v1, v1, v76, v77
	v_mfma_f32_32x32x16_bf16 v[2:17], v[168:171], v[236:239], v[2:17]
	v_max3_f32 v1, v1, v78, v79
	v_max3_f32 v1, v1, v80, v81
	v_mov_b32_e32 v162, v1
	s_nop 1
	v_permlane32_swap_b32_e32 v1, v162
	v_max_f32_e32 v162, v162, v162
	v_max_f32_e32 v1, v1, v1
	v_max_f32_e32 v1, v1, v162
	v_max_f32_e32 v162, v166, v166
	v_max_f32_e32 v162, v162, v1
	v_sub_f32_e32 v163, v1, v166
	v_mfma_f32_32x32x16_bf16 v[2:17], v[224:227], v[244:247], v[2:17]
	v_sub_f32_e32 v1, v166, v162
	v_mul_f32_e32 v1, 0x3e0293ee, v1
	v_exp_f32_e32 v1, v1
	v_cmp_ge_f32_e32 vcc, s5, v163
	s_cmp_eq_u64 vcc, exec
	s_cselect_b64 s[2:3], -1, 0
	s_barrier
	s_waitcnt vmcnt(4)
	v_cndmask_b32_e64 v224, v1, 1.0, s[2:3]
	v_cmp_gt_f32_e32 vcc, 1.0, v224
	s_waitcnt vmcnt(4)
	ds_write_b128 v202, v[130:133]
	ds_write_b128 v203, v[134:137]
	ds_write_b128 v204, v[138:141] offset:32768
	ds_write_b128 v205, v[142:145] offset:32768
	s_cbranch_vccz .LBB0_1206
	s_and_saveexec_b64 s[14:15], s[0:1]
	ds_write_b32 v194, v224 offset:128
	s_or_b64 exec, exec, s[14:15]
	s_waitcnt lgkmcnt(0)
	v_add_u32_e32 v1, v196, v178
	ds_read_b128 v[168:171], v1 offset:224
	ds_read_b128 v[172:175], v1 offset:192
	ds_read_b128 v[226:229], v1 offset:160
	ds_read_b128 v[230:233], v1 offset:128
	s_waitcnt lgkmcnt(3)
	v_pk_mul_f32 v[46:47], v[46:47], v[168:169]
	s_waitcnt lgkmcnt(2)
	v_pk_mul_f32 v[42:43], v[42:43], v[172:173]
	s_waitcnt lgkmcnt(1)
	v_pk_mul_f32 v[38:39], v[38:39], v[226:227]
	v_pk_mul_f32 v[48:49], v[48:49], v[170:171]
	v_pk_mul_f32 v[44:45], v[44:45], v[174:175]
	v_pk_mul_f32 v[40:41], v[40:41], v[228:229]
	s_waitcnt lgkmcnt(0)
	v_pk_mul_f32 v[36:37], v[36:37], v[232:233]
	v_pk_mul_f32 v[34:35], v[34:35], v[230:231]
	v_pk_mul_f32 v[62:63], v[62:63], v[168:169]
	v_pk_mul_f32 v[58:59], v[58:59], v[172:173]
	v_pk_mul_f32 v[54:55], v[54:55], v[226:227]
	v_pk_mul_f32 v[64:65], v[64:65], v[170:171]
	v_pk_mul_f32 v[60:61], v[60:61], v[174:175]
	v_pk_mul_f32 v[56:57], v[56:57], v[228:229]
	v_pk_mul_f32 v[52:53], v[52:53], v[232:233]
	v_pk_mul_f32 v[50:51], v[50:51], v[230:231]
	v_pk_mul_f32 v[30:31], v[30:31], v[168:169]
	v_pk_mul_f32 v[26:27], v[26:27], v[172:173]
	v_pk_mul_f32 v[22:23], v[22:23], v[226:227]
	v_pk_mul_f32 v[32:33], v[32:33], v[170:171]
	v_pk_mul_f32 v[28:29], v[28:29], v[174:175]
	v_pk_mul_f32 v[24:25], v[24:25], v[228:229]
	v_pk_mul_f32 v[20:21], v[20:21], v[232:233]
	v_pk_mul_f32 v[18:19], v[18:19], v[230:231]
	v_pk_mul_f32 v[14:15], v[14:15], v[168:169]
	v_pk_mul_f32 v[10:11], v[10:11], v[172:173]
	v_pk_mul_f32 v[6:7], v[6:7], v[226:227]
	v_pk_mul_f32 v[16:17], v[16:17], v[170:171]
	v_pk_mul_f32 v[12:13], v[12:13], v[174:175]
	v_pk_mul_f32 v[8:9], v[8:9], v[228:229]
	v_pk_mul_f32 v[4:5], v[4:5], v[232:233]
	v_pk_mul_f32 v[2:3], v[2:3], v[230:231]

.LBB0_1208:
	ds_read_b64_tr_b16 v[228:229], v197 offset:0
	ds_read_b64_tr_b16 v[230:231], v197 offset:0x800
	ds_read_b64_tr_b16 v[232:233], v197 offset:0x1000
	ds_read_b64_tr_b16 v[234:235], v197 offset:0x1800
	ds_read_b64_tr_b16 v[236:237], v197 offset:0x2000
	ds_read_b64_tr_b16 v[238:239], v197 offset:0x2800
	ds_read_b64_tr_b16 v[240:241], v197 offset:0x3000
	ds_read_b64_tr_b16 v[242:243], v197 offset:0x3800
	s_waitcnt lgkmcnt(0)
	s_nop 0
	v_mfma_f32_32x32x16_bf16 v[34:49], v[162:165], v[228:231], v[34:49]
	ds_read_b64_tr_b16 v[228:229], v197 offset:0x200
	ds_read_b64_tr_b16 v[230:231], v197 offset:0xa00
	v_mfma_f32_32x32x16_bf16 v[34:49], v[166:169], v[232:235], v[34:49]
	ds_read_b64_tr_b16 v[232:233], v197 offset:0x1200
	ds_read_b64_tr_b16 v[234:235], v197 offset:0x1a00
	v_mfma_f32_32x32x16_bf16 v[34:49], v[170:173], v[236:239], v[34:49]
	ds_read_b64_tr_b16 v[236:237], v197 offset:0x2200
	ds_read_b64_tr_b16 v[238:239], v197 offset:0x2a00
	ds_read_b64_tr_b16 v[244:245], v197 offset:0x3200
	ds_read_b64_tr_b16 v[246:247], v197 offset:0x3a00
	v_mfma_f32_32x32x16_bf16 v[34:49], v[174:177], v[240:243], v[34:49]
	s_waitcnt lgkmcnt(0)
	v_mfma_f32_32x32x16_bf16 v[50:65], v[162:165], v[228:231], v[50:65]
	ds_read_b64_tr_b16 v[228:229], v197 offset:0x400
	ds_read_b64_tr_b16 v[230:231], v197 offset:0xc00
	v_mfma_f32_32x32x16_bf16 v[50:65], v[166:169], v[232:235], v[50:65]
	ds_read_b64_tr_b16 v[232:233], v197 offset:0x1400
	ds_read_b64_tr_b16 v[234:235], v197 offset:0x1c00
	v_mfma_f32_32x32x16_bf16 v[50:65], v[170:173], v[236:239], v[50:65]
	ds_read_b64_tr_b16 v[236:237], v197 offset:0x2400
	ds_read_b64_tr_b16 v[238:239], v197 offset:0x2c00
	ds_read_b64_tr_b16 v[240:241], v197 offset:0x3400
	ds_read_b64_tr_b16 v[242:243], v197 offset:0x3c00
	v_mfma_f32_32x32x16_bf16 v[50:65], v[174:177], v[244:247], v[50:65]
	s_waitcnt lgkmcnt(0)
	v_mfma_f32_32x32x16_bf16 v[18:33], v[162:165], v[228:231], v[18:33]
	ds_read_b64_tr_b16 v[228:229], v197 offset:0x600
	ds_read_b64_tr_b16 v[230:231], v197 offset:0xe00
	v_mfma_f32_32x32x16_bf16 v[18:33], v[166:169], v[232:235], v[18:33]
	ds_read_b64_tr_b16 v[232:233], v197 offset:0x1600
	ds_read_b64_tr_b16 v[234:235], v197 offset:0x1e00
	v_mfma_f32_32x32x16_bf16 v[18:33], v[170:173], v[236:239], v[18:33]
	ds_read_b64_tr_b16 v[236:237], v197 offset:0x2600
	ds_read_b64_tr_b16 v[238:239], v197 offset:0x2e00
	ds_read_b64_tr_b16 v[244:245], v197 offset:0x3600
	ds_read_b64_tr_b16 v[246:247], v197 offset:0x3e00
	v_mfma_f32_32x32x16_bf16 v[18:33], v[174:177], v[240:243], v[18:33]
	s_waitcnt lgkmcnt(0)
	v_mfma_f32_32x32x16_bf16 v[2:17], v[162:165], v[228:231], v[2:17]
	v_max_f32_e32 v1, v83, v83
	v_max_f32_e32 v193, v82, v82
	v_max_f32_e32 v1, v193, v1
	v_max3_f32 v1, v1, v84, v85
	v_max3_f32 v1, v1, v86, v87
	v_max3_f32 v1, v1, v88, v89
	v_max3_f32 v1, v1, v90, v91
	v_max3_f32 v1, v1, v92, v93
	v_mfma_f32_32x32x16_bf16 v[2:17], v[166:169], v[232:235], v[2:17]
	v_max3_f32 v1, v1, v94, v95
	v_max3_f32 v1, v1, v96, v97
	v_max3_f32 v1, v1, v66, v67
	v_max3_f32 v1, v1, v68, v69
	v_max3_f32 v1, v1, v70, v71
	v_max3_f32 v1, v1, v72, v73
	v_max3_f32 v1, v1, v74, v75
	v_max3_f32 v1, v1, v76, v77
	v_mfma_f32_32x32x16_bf16 v[2:17], v[170:173], v[236:239], v[2:17]
	v_max3_f32 v1, v1, v78, v79
	v_max3_f32 v1, v1, v80, v81
	v_mov_b32_e32 v162, v1
	s_nop 1
	v_permlane32_swap_b32_e32 v1, v162
	v_max_f32_e32 v162, v162, v162
	v_max_f32_e32 v1, v1, v1
	v_max_f32_e32 v1, v1, v162
	v_max_f32_e32 v163, v225, v225
	v_max_f32_e32 v163, v163, v1
	v_sub_f32_e32 v162, v1, v225
	v_mfma_f32_32x32x16_bf16 v[2:17], v[174:177], v[244:247], v[2:17]
	v_sub_f32_e32 v1, v225, v163
	v_mul_f32_e32 v1, 0x3e0293ee, v1
	v_exp_f32_e32 v1, v1
	v_cmp_ge_f32_e32 vcc, s5, v162
	s_cmp_eq_u64 vcc, exec
	s_cselect_b64 s[2:3], -1, 0
	s_barrier
	s_waitcnt vmcnt(4)
	v_cndmask_b32_e64 v162, v1, 1.0, s[2:3]
	v_cmp_gt_f32_e32 vcc, 1.0, v162
	ds_write_b128 v202, v[146:149] offset:16384
	ds_write_b128 v203, v[150:153] offset:16384
	ds_write_b128 v204, v[154:157] offset:49152
	ds_write_b128 v205, v[158:161] offset:49152
	s_cbranch_vccz .LBB0_1212
	s_and_saveexec_b64 s[34:35], s[0:1]
	ds_write_b32 v194, v162 offset:128
	s_or_b64 exec, exec, s[34:35]
	s_waitcnt lgkmcnt(0)
	v_add_u32_e32 v1, v196, v178
	ds_read_b128 v[146:149], v1 offset:224
	ds_read_b128 v[150:153], v1 offset:192
	ds_read_b128 v[154:157], v1 offset:160
	ds_read_b128 v[158:161], v1 offset:128
	s_waitcnt lgkmcnt(3)
	v_pk_mul_f32 v[46:47], v[46:47], v[146:147]
	s_waitcnt lgkmcnt(2)
	v_pk_mul_f32 v[42:43], v[42:43], v[150:151]
	s_waitcnt lgkmcnt(1)
	v_pk_mul_f32 v[38:39], v[38:39], v[154:155]
	v_pk_mul_f32 v[48:49], v[48:49], v[148:149]
	v_pk_mul_f32 v[44:45], v[44:45], v[152:153]
	v_pk_mul_f32 v[40:41], v[40:41], v[156:157]
	s_waitcnt lgkmcnt(0)
	v_pk_mul_f32 v[36:37], v[36:37], v[160:161]
	v_pk_mul_f32 v[34:35], v[34:35], v[158:159]
	v_pk_mul_f32 v[62:63], v[62:63], v[146:147]
	v_pk_mul_f32 v[58:59], v[58:59], v[150:151]
	v_pk_mul_f32 v[54:55], v[54:55], v[154:155]
	v_pk_mul_f32 v[64:65], v[64:65], v[148:149]
	v_pk_mul_f32 v[60:61], v[60:61], v[152:153]
	v_pk_mul_f32 v[56:57], v[56:57], v[156:157]
	v_pk_mul_f32 v[52:53], v[52:53], v[160:161]
	v_pk_mul_f32 v[50:51], v[50:51], v[158:159]
	v_pk_mul_f32 v[30:31], v[30:31], v[146:147]
	v_pk_mul_f32 v[26:27], v[26:27], v[150:151]
	v_pk_mul_f32 v[22:23], v[22:23], v[154:155]
	v_pk_mul_f32 v[32:33], v[32:33], v[148:149]
	v_pk_mul_f32 v[28:29], v[28:29], v[152:153]
	v_pk_mul_f32 v[24:25], v[24:25], v[156:157]
	v_pk_mul_f32 v[20:21], v[20:21], v[160:161]
	v_pk_mul_f32 v[18:19], v[18:19], v[158:159]
	v_pk_mul_f32 v[14:15], v[14:15], v[146:147]
	v_pk_mul_f32 v[10:11], v[10:11], v[150:151]
	v_pk_mul_f32 v[6:7], v[6:7], v[154:155]
	v_pk_mul_f32 v[16:17], v[16:17], v[148:149]
	v_pk_mul_f32 v[12:13], v[12:13], v[152:153]
	v_pk_mul_f32 v[8:9], v[8:9], v[156:157]
	v_pk_mul_f32 v[4:5], v[4:5], v[160:161]
	v_pk_mul_f32 v[2:3], v[2:3], v[158:159]

.LBB0_1214:
	ds_read_b128 v[66:69], v206 offset:49152
	ds_read_b128 v[70:73], v206 offset:57344
	v_exp_f32_e32 v1, v156
	v_exp_f32_e32 v156, v157
	v_exp_f32_e32 v154, v154
	s_waitcnt lgkmcnt(1)
	v_mfma_f32_32x32x16_bf16 v[82:97], v[66:69], v[126:129], 0
	v_exp_f32_e32 v155, v155
	v_exp_f32_e32 v150, v150
	s_waitcnt lgkmcnt(0)
	v_mfma_f32_32x32x16_bf16 v[66:81], v[70:73], v[126:129], 0
	ds_read_b128 v[126:129], v207 offset:49152
	ds_read_b128 v[130:133], v207 offset:57344
	ds_read_b128 v[134:137], v208 offset:49152
	ds_read_b128 v[138:141], v208 offset:57344
	s_waitcnt lgkmcnt(3)
	v_mfma_f32_32x32x16_bf16 v[82:97], v[126:129], v[122:125], v[82:97]
	ds_read_b128 v[126:129], v209 offset:49152
	ds_read_b128 v[142:145], v209 offset:57344
	ds_read_b128 v[230:233], v210 offset:49152
	ds_read_b128 v[234:237], v210 offset:57344
	ds_read_b128 v[238:241], v211 offset:49152
	ds_read_b128 v[242:245], v211 offset:57344
	ds_read_b128 v[246:249], v212 offset:49152
	ds_read_b128 v[250:253], v212 offset:57344
	s_waitcnt lgkmcnt(10)
	v_mfma_f32_32x32x16_bf16 v[66:81], v[130:133], v[122:125], v[66:81]
	ds_read_b128 v[122:125], v213 offset:49152
	ds_read_b128 v[130:133], v213 offset:57344
	s_waitcnt lgkmcnt(11)
	v_mfma_f32_32x32x16_bf16 v[82:97], v[134:137], v[118:121], v[82:97]
	v_exp_f32_e32 v134, v151
	v_exp_f32_e32 v135, v148
	v_exp_f32_e32 v136, v149
	v_exp_f32_e32 v137, v146
	v_exp_f32_e32 v146, v147
	v_exp_f32_e32 v147, v160
	v_exp_f32_e32 v148, v161
	s_waitcnt lgkmcnt(10)
	v_mfma_f32_32x32x16_bf16 v[66:81], v[138:141], v[118:121], v[66:81]
	v_add_f32_e32 v118, 0, v177
	v_add_f32_e32 v118, v228, v118
	v_add_f32_e32 v118, v163, v118
	v_add_f32_e32 v118, v225, v118
	v_add_f32_e32 v118, v164, v118
	v_add_f32_e32 v118, v176, v118
	v_add_f32_e32 v118, v165, v118
	s_waitcnt lgkmcnt(9)
	v_mfma_f32_32x32x16_bf16 v[82:97], v[126:129], v[114:117], v[82:97]
	v_add_f32_e32 v118, v175, v118
	v_add_f32_e32 v118, v172, v118
	v_add_f32_e32 v118, v174, v118
	v_exp_f32_e32 v120, v158
	v_exp_f32_e32 v121, v159
	v_exp_f32_e32 v138, v152
	v_exp_f32_e32 v139, v153
	s_waitcnt lgkmcnt(8)
	v_mfma_f32_32x32x16_bf16 v[66:81], v[142:145], v[114:117], v[66:81]
	v_add_f32_e32 v114, v171, v118
	v_add_f32_e32 v114, v173, v114
	v_add_f32_e32 v114, v168, v114
	v_add_f32_e32 v114, v170, v114
	v_add_f32_e32 v114, v167, v114
	v_add_f32_e32 v114, v169, v114
	v_add_f32_e32 v114, v1, v114
	s_waitcnt lgkmcnt(7)
	v_mfma_f32_32x32x16_bf16 v[82:97], v[230:233], v[110:113], v[82:97]
	v_add_f32_e32 v114, v156, v114
	v_add_f32_e32 v114, v154, v114
	v_add_f32_e32 v114, v155, v114
	v_add_f32_e32 v114, v150, v114
	v_add_f32_e32 v114, v134, v114
	v_add_f32_e32 v114, v135, v114
	v_add_f32_e32 v114, v136, v114
	s_waitcnt lgkmcnt(6)
	v_mfma_f32_32x32x16_bf16 v[66:81], v[234:237], v[110:113], v[66:81]
	v_add_f32_e32 v110, v137, v114
	v_add_f32_e32 v110, v146, v110
	v_add_f32_e32 v110, v147, v110
	v_add_f32_e32 v110, v148, v110
	v_add_f32_e32 v110, v120, v110
	v_add_f32_e32 v110, v121, v110
	v_add_f32_e32 v110, v138, v110
	s_waitcnt lgkmcnt(5)
	v_mfma_f32_32x32x16_bf16 v[82:97], v[238:241], v[106:109], v[82:97]
	v_add_f32_e32 v110, v139, v110
	v_mov_b32_e32 v111, v110
	s_nop 1
	v_permlane32_swap_b32_e32 v110, v111
	v_cvt_pk_bf16_f32 v112, v177, v228
	v_cvt_pk_bf16_f32 v113, v163, v225
	v_cvt_pk_bf16_f32 v114, v164, v176
	s_waitcnt lgkmcnt(4)
	v_mfma_f32_32x32x16_bf16 v[66:81], v[242:245], v[106:109], v[66:81]
	v_cvt_pk_bf16_f32 v115, v165, v175
	v_cvt_pk_bf16_f32 v106, v172, v174
	v_cvt_pk_bf16_f32 v107, v171, v173
	v_cvt_pk_bf16_f32 v108, v168, v170
	v_cvt_pk_bf16_f32 v109, v167, v169
	v_cvt_pk_bf16_f32 v116, v1, v156
	v_cvt_pk_bf16_f32 v117, v154, v155
	s_waitcnt lgkmcnt(3)
	v_mfma_f32_32x32x16_bf16 v[82:97], v[246:249], v[102:105], v[82:97]
	v_cvt_pk_bf16_f32 v118, v150, v134
	v_cvt_pk_bf16_f32 v119, v135, v136
	v_permlane32_swap_b32_e32 v112, v114
	v_permlane32_swap_b32_e32 v113, v115
	v_permlane32_swap_b32_e32 v106, v108
	s_waitcnt lgkmcnt(2)
	v_mfma_f32_32x32x16_bf16 v[66:81], v[250:253], v[102:105], v[66:81]
	v_cvt_pk_bf16_f32 v102, v137, v146
	v_cvt_pk_bf16_f32 v103, v147, v148
	v_cvt_pk_bf16_f32 v104, v120, v121
	v_cvt_pk_bf16_f32 v105, v138, v139
	v_permlane32_swap_b32_e32 v107, v109
	v_permlane32_swap_b32_e32 v116, v118
	s_waitcnt lgkmcnt(1)
	v_mfma_f32_32x32x16_bf16 v[82:97], v[122:125], v[98:101], v[82:97]
	v_permlane32_swap_b32_e32 v117, v119
	v_permlane32_swap_b32_e32 v102, v104
	v_permlane32_swap_b32_e32 v103, v105
	s_waitcnt lgkmcnt(0)
	v_mfma_f32_32x32x16_bf16 v[66:81], v[130:133], v[98:101], v[66:81]
	ds_read_b64_tr_b16 v[98:99], v195 offset:0
	ds_read_b64_tr_b16 v[100:101], v195 offset:0x800
	ds_read_b64_tr_b16 v[120:121], v195 offset:0x1000
	ds_read_b64_tr_b16 v[122:123], v195 offset:0x1800
	ds_read_b64_tr_b16 v[124:125], v195 offset:0x2000
	ds_read_b64_tr_b16 v[126:127], v195 offset:0x2800
	ds_read_b64_tr_b16 v[128:129], v195 offset:0x3000
	ds_read_b64_tr_b16 v[130:131], v195 offset:0x3800
	s_waitcnt lgkmcnt(0)
	s_nop 0
	v_mfma_f32_32x32x16_bf16 v[34:49], v[112:115], v[98:101], v[34:49]
	ds_read_b64_tr_b16 v[98:99], v195 offset:0x200
	ds_read_b64_tr_b16 v[100:101], v195 offset:0xa00
	v_mfma_f32_32x32x16_bf16 v[34:49], v[106:109], v[120:123], v[34:49]
	ds_read_b64_tr_b16 v[120:121], v195 offset:0x1200
	ds_read_b64_tr_b16 v[122:123], v195 offset:0x1a00
	v_mfma_f32_32x32x16_bf16 v[34:49], v[116:119], v[124:127], v[34:49]
	ds_read_b64_tr_b16 v[124:125], v195 offset:0x2200
	ds_read_b64_tr_b16 v[126:127], v195 offset:0x2a00
	ds_read_b64_tr_b16 v[132:133], v195 offset:0x3200
	ds_read_b64_tr_b16 v[134:135], v195 offset:0x3a00
	v_mfma_f32_32x32x16_bf16 v[34:49], v[102:105], v[128:131], v[34:49]
	s_waitcnt lgkmcnt(0)
	v_mfma_f32_32x32x16_bf16 v[50:65], v[112:115], v[98:101], v[50:65]
	ds_read_b64_tr_b16 v[98:99], v195 offset:0x400
	ds_read_b64_tr_b16 v[100:101], v195 offset:0xc00
	v_mfma_f32_32x32x16_bf16 v[50:65], v[106:109], v[120:123], v[50:65]
	ds_read_b64_tr_b16 v[120:121], v195 offset:0x1400
	ds_read_b64_tr_b16 v[122:123], v195 offset:0x1c00
	v_mfma_f32_32x32x16_bf16 v[50:65], v[116:119], v[124:127], v[50:65]
	ds_read_b64_tr_b16 v[124:125], v195 offset:0x2400
	ds_read_b64_tr_b16 v[126:127], v195 offset:0x2c00
	ds_read_b64_tr_b16 v[128:129], v195 offset:0x3400
	ds_read_b64_tr_b16 v[130:131], v195 offset:0x3c00
	v_mfma_f32_32x32x16_bf16 v[50:65], v[102:105], v[132:135], v[50:65]
	s_waitcnt lgkmcnt(0)
	v_mfma_f32_32x32x16_bf16 v[18:33], v[112:115], v[98:101], v[18:33]
	ds_read_b64_tr_b16 v[98:99], v195 offset:0x600
	ds_read_b64_tr_b16 v[100:101], v195 offset:0xe00
	v_mfma_f32_32x32x16_bf16 v[18:33], v[106:109], v[120:123], v[18:33]
	ds_read_b64_tr_b16 v[120:121], v195 offset:0x1600
	ds_read_b64_tr_b16 v[122:123], v195 offset:0x1e00
	v_mfma_f32_32x32x16_bf16 v[18:33], v[116:119], v[124:127], v[18:33]
	ds_read_b64_tr_b16 v[124:125], v195 offset:0x2600
	ds_read_b64_tr_b16 v[126:127], v195 offset:0x2e00
	ds_read_b64_tr_b16 v[132:133], v195 offset:0x3600
	ds_read_b64_tr_b16 v[134:135], v195 offset:0x3e00
	v_mfma_f32_32x32x16_bf16 v[18:33], v[102:105], v[128:131], v[18:33]
	s_waitcnt lgkmcnt(0)
	v_mfma_f32_32x32x16_bf16 v[2:17], v[112:115], v[98:101], v[2:17]
	v_max_f32_e32 v1, v83, v83
	v_max_f32_e32 v128, v82, v82
	v_max_f32_e32 v1, v128, v1
	v_max3_f32 v1, v1, v84, v85
	v_max3_f32 v1, v1, v86, v87
	v_max3_f32 v1, v1, v88, v89
	v_max3_f32 v1, v1, v90, v91
	v_max3_f32 v1, v1, v92, v93
	v_mfma_f32_32x32x16_bf16 v[2:17], v[106:109], v[120:123], v[2:17]
	v_max3_f32 v1, v1, v94, v95
	v_max3_f32 v1, v1, v96, v97
	v_max3_f32 v1, v1, v66, v67
	v_max3_f32 v1, v1, v68, v69
	v_max3_f32 v1, v1, v70, v71
	v_max3_f32 v1, v1, v72, v73
	v_max3_f32 v1, v1, v74, v75
	v_max3_f32 v1, v1, v76, v77
	v_mfma_f32_32x32x16_bf16 v[2:17], v[116:119], v[124:127], v[2:17]
	v_max3_f32 v1, v1, v78, v79
	v_max3_f32 v1, v1, v80, v81
	v_mov_b32_e32 v98, v1
	s_nop 1
	v_permlane32_swap_b32_e32 v1, v98
	v_max_f32_e32 v98, v98, v98
	v_max_f32_e32 v1, v1, v1
	v_max_f32_e32 v1, v1, v98
	v_max_f32_e32 v99, v166, v166
	v_max_f32_e32 v99, v99, v1
	v_sub_f32_e32 v98, v1, v166
	v_mfma_f32_32x32x16_bf16 v[2:17], v[102:105], v[132:135], v[2:17]
	v_sub_f32_e32 v1, v166, v99
	v_mul_f32_e32 v1, 0x3e0293ee, v1
	v_exp_f32_e32 v1, v1
	v_cmp_ge_f32_e32 vcc, s5, v98
	s_cmp_eq_u64 vcc, exec
	s_cselect_b64 s[2:3], -1, 0
	v_cndmask_b32_e64 v98, v1, 1.0, s[2:3]
	v_cmp_gt_f32_e32 vcc, 1.0, v98
	s_barrier
	s_cbranch_vccz .LBB0_1218
	s_and_saveexec_b64 s[10:11], s[0:1]
	ds_write_b32 v194, v98 offset:128
	s_or_b64 exec, exec, s[10:11]
	s_waitcnt lgkmcnt(0)
	v_add_u32_e32 v1, v196, v178
	ds_read_b128 v[100:103], v1 offset:224
	ds_read_b128 v[104:107], v1 offset:192
	ds_read_b128 v[112:115], v1 offset:160
	ds_read_b128 v[116:119], v1 offset:128
	s_waitcnt lgkmcnt(3)
	v_pk_mul_f32 v[46:47], v[46:47], v[100:101]
	s_waitcnt lgkmcnt(2)
	v_pk_mul_f32 v[42:43], v[42:43], v[104:105]
	s_waitcnt lgkmcnt(1)
	v_pk_mul_f32 v[38:39], v[38:39], v[112:113]
	v_pk_mul_f32 v[48:49], v[48:49], v[102:103]
	v_pk_mul_f32 v[44:45], v[44:45], v[106:107]
	v_pk_mul_f32 v[40:41], v[40:41], v[114:115]
	s_waitcnt lgkmcnt(0)
	v_pk_mul_f32 v[36:37], v[36:37], v[118:119]
	v_pk_mul_f32 v[34:35], v[34:35], v[116:117]
	v_pk_mul_f32 v[62:63], v[62:63], v[100:101]
	v_pk_mul_f32 v[58:59], v[58:59], v[104:105]
	v_pk_mul_f32 v[54:55], v[54:55], v[112:113]
	v_pk_mul_f32 v[64:65], v[64:65], v[102:103]
	v_pk_mul_f32 v[60:61], v[60:61], v[106:107]
	v_pk_mul_f32 v[56:57], v[56:57], v[114:115]
	v_pk_mul_f32 v[52:53], v[52:53], v[118:119]
	v_pk_mul_f32 v[50:51], v[50:51], v[116:117]
	v_pk_mul_f32 v[30:31], v[30:31], v[100:101]
	v_pk_mul_f32 v[26:27], v[26:27], v[104:105]
	v_pk_mul_f32 v[22:23], v[22:23], v[112:113]
	v_pk_mul_f32 v[32:33], v[32:33], v[102:103]
	v_pk_mul_f32 v[28:29], v[28:29], v[106:107]
	v_pk_mul_f32 v[24:25], v[24:25], v[114:115]
	v_pk_mul_f32 v[20:21], v[20:21], v[118:119]
	v_pk_mul_f32 v[18:19], v[18:19], v[116:117]
	v_pk_mul_f32 v[14:15], v[14:15], v[100:101]
	v_pk_mul_f32 v[10:11], v[10:11], v[104:105]
	v_pk_mul_f32 v[6:7], v[6:7], v[112:113]
	v_pk_mul_f32 v[16:17], v[16:17], v[102:103]
	v_pk_mul_f32 v[12:13], v[12:13], v[106:107]
	v_pk_mul_f32 v[8:9], v[8:9], v[114:115]
	v_pk_mul_f32 v[4:5], v[4:5], v[118:119]
	v_pk_mul_f32 v[2:3], v[2:3], v[116:117]
.LBB0_1218:
	v_cndmask_b32_e64 v1, v99, v166, s[2:3]
	v_mul_f32_e32 v99, 0xbe0293ee, v1
	v_fmamk_f32 v1, v82, 0x3e0293ee, v99
	v_fmamk_f32 v82, v83, 0x3e0293ee, v99
	v_fmamk_f32 v83, v84, 0x3e0293ee, v99
	v_exp_f32_e32 v84, v1
	v_fmamk_f32 v100, v86, 0x3e0293ee, v99
	v_exp_f32_e32 v86, v82
	v_fmamk_f32 v85, v85, 0x3e0293ee, v99
	v_exp_f32_e32 v82, v83
	v_fmamk_f32 v66, v66, 0x3e0293ee, v99
	v_exp_f32_e32 v85, v85
	v_fmamk_f32 v101, v87, 0x3e0293ee, v99
	v_fmamk_f32 v112, v96, 0x3e0293ee, v99
	v_fmamk_f32 v96, v77, 0x3e0293ee, v99
	v_exp_f32_e32 v77, v100
	v_exp_f32_e32 v1, v66
	v_add_f32_e32 v66, 0, v84
	v_fmamk_f32 v102, v88, 0x3e0293ee, v99
	v_exp_f32_e32 v83, v101
	v_add_f32_e32 v66, v86, v66
	v_fmamk_f32 v103, v89, 0x3e0293ee, v99
	v_fmamk_f32 v109, v95, 0x3e0293ee, v99
	v_fmamk_f32 v95, v76, 0x3e0293ee, v99
	v_exp_f32_e32 v76, v102
	v_add_f32_e32 v66, v82, v66
	v_fmamk_f32 v104, v90, 0x3e0293ee, v99
	v_fmamk_f32 v113, v97, 0x3e0293ee, v99
	v_fmamk_f32 v97, v78, 0x3e0293ee, v99
	v_exp_f32_e32 v78, v103
	v_add_f32_e32 v66, v85, v66
	v_fmamk_f32 v105, v91, 0x3e0293ee, v99
	v_fmamk_f32 v106, v92, 0x3e0293ee, v99
	v_fmamk_f32 v92, v73, 0x3e0293ee, v99
	v_exp_f32_e32 v73, v104
	v_add_f32_e32 v66, v77, v66
	v_fmamk_f32 v108, v94, 0x3e0293ee, v99
	v_fmamk_f32 v94, v75, 0x3e0293ee, v99
	v_exp_f32_e32 v75, v105
	v_add_f32_e32 v66, v83, v66
	v_fmamk_f32 v107, v93, 0x3e0293ee, v99
	v_fmamk_f32 v90, v71, 0x3e0293ee, v99
	v_exp_f32_e32 v71, v106
	v_add_f32_e32 v66, v76, v66
	v_fmamk_f32 v93, v74, 0x3e0293ee, v99
	v_exp_f32_e32 v74, v107
	v_add_f32_e32 v66, v78, v66
	v_fmamk_f32 v88, v69, 0x3e0293ee, v99
	v_exp_f32_e32 v69, v108
	v_add_f32_e32 v66, v73, v66
	v_fmamk_f32 v91, v72, 0x3e0293ee, v99
	v_exp_f32_e32 v72, v109
	v_add_f32_e32 v66, v75, v66
	v_fmamk_f32 v87, v68, 0x3e0293ee, v99
	v_exp_f32_e32 v68, v112
	v_add_f32_e32 v66, v71, v66
	v_fmamk_f32 v89, v70, 0x3e0293ee, v99
	v_exp_f32_e32 v70, v113
	v_add_f32_e32 v66, v74, v66
	v_fmamk_f32 v67, v67, 0x3e0293ee, v99
	v_add_f32_e32 v66, v69, v66
	v_exp_f32_e32 v100, v67
	v_add_f32_e32 v66, v72, v66
	v_exp_f32_e32 v87, v87
	v_add_f32_e32 v66, v68, v66
	v_exp_f32_e32 v88, v88
	v_add_f32_e32 v66, v70, v66
	v_exp_f32_e32 v89, v89
	v_add_f32_e32 v66, v1, v66
	v_exp_f32_e32 v90, v90
	v_add_f32_e32 v66, v100, v66
	v_exp_f32_e32 v91, v91
	v_add_f32_e32 v66, v87, v66
	v_exp_f32_e32 v92, v92
	v_add_f32_e32 v66, v88, v66
	v_exp_f32_e32 v93, v93
	v_add_f32_e32 v66, v89, v66
	v_exp_f32_e32 v94, v94
	v_add_f32_e32 v66, v90, v66
	v_exp_f32_e32 v95, v95
	v_add_f32_e32 v66, v91, v66
	v_exp_f32_e32 v96, v96
	v_add_f32_e32 v66, v92, v66
	v_fmamk_f32 v79, v79, 0x3e0293ee, v99
	v_exp_f32_e32 v97, v97
	v_add_f32_e32 v66, v93, v66
	v_fmamk_f32 v80, v80, 0x3e0293ee, v99
	v_exp_f32_e32 v101, v79
	v_add_f32_e32 v66, v94, v66
	v_fmac_f32_e32 v99, 0x3e0293ee, v81
	v_exp_f32_e32 v102, v80
	v_add_f32_e32 v66, v95, v66
	v_exp_f32_e32 v99, v99
	v_add_f32_e32 v66, v96, v66
	v_add_f32_e32 v66, v97, v66
	v_add_f32_e32 v66, v101, v66
	v_add_f32_e32 v66, v102, v66
	v_add_f32_e32 v66, v99, v66
	v_mov_b32_e32 v67, v66
	s_nop 1
	v_permlane32_swap_b32_e32 v66, v67
	v_cvt_pk_bf16_f32 v80, v84, v86
	v_cvt_pk_bf16_f32 v81, v82, v85
	v_cvt_pk_bf16_f32 v82, v77, v83
	v_cvt_pk_bf16_f32 v83, v76, v78
	v_cvt_pk_bf16_f32 v76, v73, v75
	v_cvt_pk_bf16_f32 v77, v71, v74
	v_cvt_pk_bf16_f32 v78, v69, v72
	v_cvt_pk_bf16_f32 v79, v68, v70
	v_cvt_pk_bf16_f32 v68, v1, v100
	v_cvt_pk_bf16_f32 v69, v87, v88
	v_cvt_pk_bf16_f32 v70, v89, v90
	v_cvt_pk_bf16_f32 v71, v91, v92
	v_cvt_pk_bf16_f32 v72, v93, v94
	v_cvt_pk_bf16_f32 v73, v95, v96
	v_cvt_pk_bf16_f32 v74, v97, v101
	v_cvt_pk_bf16_f32 v75, v102, v99
	s_nop 0
	v_permlane32_swap_b32_e32 v80, v82
	v_permlane32_swap_b32_e32 v81, v83
	v_permlane32_swap_b32_e32 v76, v78
	v_permlane32_swap_b32_e32 v77, v79
	v_permlane32_swap_b32_e32 v68, v70
	v_permlane32_swap_b32_e32 v69, v71
	v_permlane32_swap_b32_e32 v72, v74
	v_permlane32_swap_b32_e32 v73, v75
	ds_read_b64_tr_b16 v[84:85], v197 offset:0
	ds_read_b64_tr_b16 v[86:87], v197 offset:0x800
	ds_read_b64_tr_b16 v[88:89], v197 offset:0x1000
	ds_read_b64_tr_b16 v[90:91], v197 offset:0x1800
	ds_read_b64_tr_b16 v[92:93], v197 offset:0x2000
	ds_read_b64_tr_b16 v[94:95], v197 offset:0x2800
	ds_read_b64_tr_b16 v[100:101], v197 offset:0x3000
	ds_read_b64_tr_b16 v[102:103], v197 offset:0x3800
	s_waitcnt lgkmcnt(0)
	s_nop 0
	v_mfma_f32_32x32x16_bf16 v[34:49], v[80:83], v[84:87], v[34:49]
	ds_read_b64_tr_b16 v[84:85], v197 offset:0x200
	ds_read_b64_tr_b16 v[86:87], v197 offset:0xa00
	v_mfma_f32_32x32x16_bf16 v[34:49], v[76:79], v[88:91], v[34:49]
	ds_read_b64_tr_b16 v[88:89], v197 offset:0x1200
	ds_read_b64_tr_b16 v[90:91], v197 offset:0x1a00
	v_mfma_f32_32x32x16_bf16 v[34:49], v[68:71], v[92:95], v[34:49]
	ds_read_b64_tr_b16 v[92:93], v197 offset:0x2200
	ds_read_b64_tr_b16 v[94:95], v197 offset:0x2a00
	ds_read_b64_tr_b16 v[104:105], v197 offset:0x3200
	ds_read_b64_tr_b16 v[106:107], v197 offset:0x3a00
	v_mfma_f32_32x32x16_bf16 v[34:49], v[72:75], v[100:103], v[34:49]
	s_waitcnt lgkmcnt(0)
	v_mfma_f32_32x32x16_bf16 v[50:65], v[80:83], v[84:87], v[50:65]
	ds_read_b64_tr_b16 v[84:85], v197 offset:0x400
	ds_read_b64_tr_b16 v[86:87], v197 offset:0xc00
	v_mfma_f32_32x32x16_bf16 v[50:65], v[76:79], v[88:91], v[50:65]
	ds_read_b64_tr_b16 v[88:89], v197 offset:0x1400
	ds_read_b64_tr_b16 v[90:91], v197 offset:0x1c00
	v_mfma_f32_32x32x16_bf16 v[50:65], v[68:71], v[92:95], v[50:65]
	ds_read_b64_tr_b16 v[92:93], v197 offset:0x2400
	ds_read_b64_tr_b16 v[94:95], v197 offset:0x2c00
	ds_read_b64_tr_b16 v[100:101], v197 offset:0x3400
	ds_read_b64_tr_b16 v[102:103], v197 offset:0x3c00
	v_mfma_f32_32x32x16_bf16 v[50:65], v[72:75], v[104:107], v[50:65]
	s_waitcnt lgkmcnt(0)
	v_mfma_f32_32x32x16_bf16 v[18:33], v[80:83], v[84:87], v[18:33]
	ds_read_b64_tr_b16 v[84:85], v197 offset:0x600
	ds_read_b64_tr_b16 v[86:87], v197 offset:0xe00
	v_mfma_f32_32x32x16_bf16 v[18:33], v[76:79], v[88:91], v[18:33]
	ds_read_b64_tr_b16 v[88:89], v197 offset:0x1600
	ds_read_b64_tr_b16 v[90:91], v197 offset:0x1e00
	v_mfma_f32_32x32x16_bf16 v[18:33], v[68:71], v[92:95], v[18:33]
	ds_read_b64_tr_b16 v[92:93], v197 offset:0x2600
	ds_read_b64_tr_b16 v[94:95], v197 offset:0x2e00
	ds_read_b64_tr_b16 v[104:105], v197 offset:0x3600
	ds_read_b64_tr_b16 v[106:107], v197 offset:0x3e00
	v_mfma_f32_32x32x16_bf16 v[18:33], v[72:75], v[100:103], v[18:33]
	s_waitcnt lgkmcnt(0)
	v_mfma_f32_32x32x16_bf16 v[2:17], v[80:83], v[84:87], v[2:17]
	v_mfma_f32_32x32x16_bf16 v[2:17], v[76:79], v[88:91], v[2:17]
	v_mfma_f32_32x32x16_bf16 v[2:17], v[68:71], v[92:95], v[2:17]
	v_mfma_f32_32x32x16_bf16 v[2:17], v[72:75], v[104:107], v[2:17]
	s_and_saveexec_b64 s[2:3], s[0:1]
	s_cbranch_execz .LBB0_1200
	v_add_f32_e32 v1, v110, v111
	v_fmac_f32_e32 v1, v220, v162
	v_add_f32_e32 v66, v66, v67
	v_fmac_f32_e32 v66, v1, v98
	ds_write_b32 v194, v66
	s_branch .LBB0_1200
